# speedup vs baseline: 1.0656x; 1.0233x over previous
_Z7k_layerILi1EEvPKDF16_S1_PKfS3_S3_S3_S3_S3_S1_S1_S1_S1_S3_S3_PKhS5_PDF16_S6_PfS7_:
	s_ashr_i32 s3, s2, 1
	s_and_b32 s3, s3, -8
	s_and_b32 s16, s2, 7
	v_readfirstlane_b32 s15, v0
	s_or_b32 s12, s3, s16
	s_bfe_u32 s14, s2, 0x10003
	s_cmpk_gt_u32 s15, 0xff
	s_mov_b64 s[2:3], -1
	s_cbranch_scc0 .LBB2_17
	s_mov_b32 s44, 0x3e000000
	v_mov_b32_e32 v240, 0x64646464
	s_mov_b32 s42, 0x4010400
	s_mov_b32 s43, 0x4030402
	s_load_dwordx2 s[4:5], s[0:1], 0x80
	s_load_dwordx2 s[8:9], s[0:1], 0x0
	v_lshlrev_b32_e32 v2, 3, v0
	v_add_u32_e32 v1, 0xffffff00, v0
	v_ashrrev_i32_e32 v3, 4, v1
	v_and_b32_e32 v38, 0x78, v2
	s_lshl_b32 s17, s12, 9
	v_add_u32_e32 v2, s17, v3
	v_lshlrev_b32_e32 v4, 1, v38
	s_mov_b32 s7, 0x20000
	s_mov_b32 s6, 0x1000000
	v_lshl_or_b32 v2, v2, 8, v4
	s_waitcnt lgkmcnt(0)
	s_and_b32 s9, s9, 0xffff
	s_mov_b32 s10, s6
	s_mov_b32 s11, s7
	v_add_u32_e32 v5, 0x4000, v2
	buffer_load_dwordx4 v[10:13], v2, s[8:11], 0 offen sc1
	buffer_load_dwordx4 v[18:21], v5, s[8:11], 0 offen sc1
	v_add_u32_e32 v5, 0x1000, v2
	buffer_load_dwordx4 v[26:29], v5, s[8:11], 0 offen sc1
	v_add_u32_e32 v5, 0x2000, v2
	v_add_u32_e32 v6, 0x3000, v2
	buffer_load_dwordx4 v[30:33], v5, s[8:11], 0 offen sc1
	buffer_load_dwordx4 v[58:61], v6, s[8:11], 0 offen sc1
	v_add_u32_e32 v5, 0x5000, v2
	buffer_load_dwordx4 v[34:37], v5, s[8:11], 0 offen sc1
	v_add_u32_e32 v5, 0x6000, v2
	v_add_u32_e32 v2, 0x7000, v2
	buffer_load_dwordx4 v[62:65], v5, s[8:11], 0 offen sc1
	buffer_load_dwordx4 v[66:69], v2, s[8:11], 0 offen sc1
	s_or_b32 s2, s17, 0x80
	v_add_u32_e32 v2, s2, v3
	v_lshl_or_b32 v6, v2, 8, v4
	v_add_u32_e32 v2, 0x1000, v6
	v_add_u32_e32 v7, 0x2000, v6
	v_add_u32_e32 v8, 0x3000, v6
	buffer_load_dwordx4 v[70:73], v6, s[8:11], 0 offen sc1
	buffer_load_dwordx4 v[74:77], v2, s[8:11], 0 offen sc1
	buffer_load_dwordx4 v[14:17], v7, s[8:11], 0 offen sc1
	s_nop 0
	buffer_load_dwordx4 v[2:5], v8, s[8:11], 0 offen sc1
	v_add_u32_e32 v7, 0x4000, v6
	v_add_u32_e32 v8, 0x5000, v6
	v_add_u32_e32 v39, 0x6000, v6
	buffer_load_dwordx4 v[78:81], v7, s[8:11], 0 offen sc1
	buffer_load_dwordx4 v[82:85], v8, s[8:11], 0 offen sc1
	v_add_u32_e32 v40, 0x7000, v6
	buffer_load_dwordx4 v[22:25], v39, s[8:11], 0 offen sc1
	buffer_load_dwordx4 v[6:9], v40, s[8:11], 0 offen sc1
	v_lshlrev_b32_e32 v48, 2, v38
	v_or_b32_e32 v38, 0x1e600, v48
	s_barrier
	ds_read_b128 v[38:41], v38
	v_or_b32_e32 v42, 0x1ea00, v48
	ds_read_b128 v[42:45], v42
	v_or_b32_e32 v49, 0x1e800, v48
	v_or_b32_e32 v50, 0x1ec00, v48
	s_waitcnt lgkmcnt(1)
	v_cvt_pk_f16_f32 v46, v38, v39
	v_or_b32_e32 v38, 0x1e610, v48
	v_cvt_pk_f16_f32 v47, v40, v41
	ds_read_b128 v[38:41], v38
	v_or_b32_e32 v51, 0x1ea10, v48
	ds_read_b128 v[54:57], v49
	ds_read_b128 v[86:89], v50
	ds_read_b128 v[90:93], v51
	v_or_b32_e32 v94, 0x1e810, v48
	v_or_b32_e32 v48, 0x1ec10, v48
	s_waitcnt lgkmcnt(3)
	v_cvt_pk_f16_f32 v51, v38, v39
	s_waitcnt lgkmcnt(2)
	v_pk_fma_f32 v[38:39], v[54:55], 0, v[42:43] op_sel_hi:[1,0,1]
	v_cvt_pk_f16_f32 v52, v40, v41
	s_waitcnt lgkmcnt(1)
	v_pk_add_f32 v[38:39], v[86:87], v[38:39]
	v_pk_fma_f32 v[42:43], v[56:57], 0, v[44:45] op_sel_hi:[1,0,1]
	v_cvt_pk_f16_f32 v53, v38, v39
	ds_read_b128 v[38:41], v94
	ds_read_b128 v[94:97], v48
	v_pk_add_f32 v[42:43], v[88:89], v[42:43]
	s_movk_i32 s13, 0x110
	v_cvt_pk_f16_f32 v55, v42, v43
	s_waitcnt lgkmcnt(1)
	v_pk_fma_f32 v[38:39], v[38:39], 0, v[90:91] op_sel_hi:[1,0,1]
	s_or_b32 s20, s17, 0x100
	s_waitcnt lgkmcnt(0)
	v_pk_add_f32 v[38:39], v[94:95], v[38:39]
	s_or_b32 s18, s17, 0x180
	v_cvt_pk_f16_f32 v56, v38, v39
	v_pk_fma_f32 v[38:39], v[40:41], 0, v[92:93] op_sel_hi:[1,0,1]
	s_lshl_b32 s17, s14, 6
	v_pk_add_f32 v[38:39], v[96:97], v[38:39]
	v_mov_b32_e32 v122, 0x11000
	v_cvt_pk_f16_f32 v57, v38, v39
	v_mov_b32_e32 v38, v0
	s_and_b32 s5, s5, 0xffff
	v_add_u32_e32 v39, 0xffffff00, v38
	v_lshlrev_b32_e32 v38, 4, v38
	v_ashrrev_i32_e32 v39, 4, v39
	v_and_b32_e32 v40, 0xf0, v38
	v_mad_u64_u32 v[42:43], s[22:23], v39, s13, v[40:41]
	s_lshl_b32 s2, s2, 7
	s_or_b32 s2, s2, s17
	s_mov_b32 s3, 0
	s_lshr_b32 s19, s15, 6
	s_movk_i32 s21, 0x1000
	s_waitcnt vmcnt(15)
	v_pk_fma_f16 v12, v51, v12, v56
	v_pk_fma_f16 v10, v46, v10, v53
	v_pk_fma_f16 v13, v52, v13, v57
	v_pk_fma_f16 v11, v47, v11, v55
	s_waitcnt vmcnt(14)
	v_pk_fma_f16 v20, v51, v20, v56
	v_pk_fma_f16 v18, v46, v18, v53
	v_pk_fma_f16 v21, v52, v21, v57
	v_pk_fma_f16 v19, v47, v19, v55
	ds_write_b128 v42, v[10:13]
	ds_write_b128 v42, v[18:21] offset:17408
	v_pk_add_f16 v44, v13, v21
	v_pk_add_f16 v48, v12, v20
	v_pk_add_f16 v54, v11, v19
	v_pk_add_f16 v114, v10, v18
	s_waitcnt vmcnt(13)
	v_pk_fma_f16 v12, v51, v28, v56
	v_pk_fma_f16 v10, v46, v26, v53
	v_pk_fma_f16 v13, v52, v29, v57
	v_pk_fma_f16 v11, v47, v27, v55
	s_waitcnt vmcnt(10)
	v_pk_fma_f16 v20, v51, v36, v56
	v_pk_fma_f16 v18, v46, v34, v53
	v_pk_fma_f16 v21, v52, v37, v57
	v_pk_fma_f16 v19, v47, v35, v55
	ds_write_b128 v42, v[10:13] offset:4352
	ds_write_b128 v42, v[18:21] offset:21760
	v_pk_add_f16 v36, v13, v21
	v_pk_add_f16 v38, v12, v20
	v_pk_add_f16 v41, v11, v19
	v_pk_add_f16 v43, v10, v18
	v_pk_fma_f16 v12, v51, v32, v56
	v_pk_fma_f16 v10, v46, v30, v53
	v_pk_fma_f16 v13, v52, v33, v57
	v_pk_fma_f16 v11, v47, v31, v55
	s_waitcnt vmcnt(9)
	v_pk_fma_f16 v20, v51, v64, v56
	v_pk_fma_f16 v18, v46, v62, v53
	v_pk_fma_f16 v21, v52, v65, v57
	v_pk_fma_f16 v19, v47, v63, v55
	ds_write_b128 v42, v[10:13] offset:8704
	ds_write_b128 v42, v[18:21] offset:26112
	v_pk_add_f16 v30, v13, v21
	v_pk_add_f16 v31, v12, v20
	v_pk_add_f16 v33, v11, v19
	v_pk_add_f16 v35, v10, v18
	v_pk_fma_f16 v12, v51, v60, v56
	v_pk_fma_f16 v10, v46, v58, v53
	v_pk_fma_f16 v13, v52, v61, v57
	v_pk_fma_f16 v11, v47, v59, v55
	s_waitcnt vmcnt(8)
	v_pk_fma_f16 v18, v46, v66, v53
	v_pk_fma_f16 v20, v51, v68, v56
	v_pk_fma_f16 v21, v52, v69, v57
	v_pk_fma_f16 v19, v47, v67, v55
	ds_write_b128 v42, v[10:13] offset:13056
	ds_write_b128 v42, v[18:21] offset:30464
	v_pk_add_f16 v29, v10, v18
	v_add_u32_e32 v10, s20, v39
	v_lshl_or_b32 v18, v10, 8, v40
	v_pk_add_f16 v28, v11, v19
	v_add_u32_e32 v10, 0x1000, v18
	v_add_u32_e32 v19, 0x2000, v18
	v_pk_add_f16 v26, v13, v21
	v_pk_add_f16 v27, v12, v20
	buffer_load_dwordx4 v[60:63], v18, s[8:11], 0 offen sc1
	buffer_load_dwordx4 v[64:67], v10, s[8:11], 0 offen sc1
	v_add_u32_e32 v20, 0x3000, v18
	buffer_load_dwordx4 v[86:89], v19, s[8:11], 0 offen sc1
	buffer_load_dwordx4 v[10:13], v20, s[8:11], 0 offen sc1
	v_add_u32_e32 v19, 0x4000, v18
	v_add_u32_e32 v20, 0x5000, v18
	buffer_load_dwordx4 v[90:93], v19, s[8:11], 0 offen sc1
	buffer_load_dwordx4 v[94:97], v20, s[8:11], 0 offen sc1
	v_add_u32_e32 v32, 0x6000, v18
	v_add_u32_e32 v34, 0x7000, v18
	buffer_load_dwordx4 v[98:101], v32, s[8:11], 0 offen sc1
	buffer_load_dwordx4 v[18:21], v34, s[8:11], 0 offen sc1
	v_mov_b32_e32 v32, v0
	s_waitcnt lgkmcnt(0)
	s_barrier
	s_waitcnt vmcnt(15)
	v_pk_fma_f16 v72, v51, v72, v56
	v_add_u32_e32 v34, 0xffffff00, v32
	v_lshlrev_b32_e32 v32, 4, v32
	v_ashrrev_i32_e32 v59, 4, v34
	v_and_b32_e32 v102, 0xf0, v32
	v_pk_fma_f16 v70, v46, v70, v53
	v_pk_fma_f16 v73, v52, v73, v57
	v_pk_fma_f16 v71, v47, v71, v55
	s_waitcnt vmcnt(11)
	v_pk_fma_f16 v78, v46, v78, v53
	v_pk_fma_f16 v79, v47, v79, v55
	v_mad_u64_u32 v[104:105], s[22:23], v59, s13, v[102:103]
	v_pk_fma_f16 v80, v51, v80, v56
	v_pk_fma_f16 v81, v52, v81, v57
	ds_write_b128 v104, v[70:73] offset:34816
	ds_write_b128 v104, v[78:81] offset:52224
	v_pk_add_f16 v117, v71, v79
	v_pk_add_f16 v118, v70, v78
	v_pk_fma_f16 v70, v51, v76, v56
	v_pk_fma_f16 v68, v46, v74, v53
	v_pk_fma_f16 v71, v52, v77, v57
	v_pk_fma_f16 v69, v47, v75, v55
	v_pk_fma_f16 v16, v51, v16, v56
	v_pk_fma_f16 v14, v46, v14, v53
	v_pk_fma_f16 v17, v52, v17, v57
	v_pk_fma_f16 v15, v47, v15, v55
	v_pk_fma_f16 v4, v51, v4, v56
	v_pk_fma_f16 v2, v46, v2, v53
	v_pk_fma_f16 v5, v52, v5, v57
	v_pk_fma_f16 v3, v47, v3, v55
	s_waitcnt vmcnt(8)
	v_pk_fma_f16 v6, v46, v6, v53
	v_pk_add_f16 v115, v73, v81
	v_pk_add_f16 v116, v72, v80
	v_pk_fma_f16 v74, v51, v84, v56
	v_pk_fma_f16 v72, v46, v82, v53
	v_pk_fma_f16 v75, v52, v85, v57
	v_pk_fma_f16 v73, v47, v83, v55
	ds_write_b128 v104, v[68:71] offset:39168
	ds_write_b128 v104, v[72:75] offset:56576
	v_pk_fma_f16 v24, v51, v24, v56
	v_pk_fma_f16 v22, v46, v22, v53
	v_pk_fma_f16 v25, v52, v25, v57
	v_pk_fma_f16 v23, v47, v23, v55
	ds_write_b128 v104, v[14:17] offset:43520
	ds_write_b128 v104, v[22:25] offset:60928
	v_pk_fma_f16 v8, v51, v8, v56
	v_pk_fma_f16 v9, v52, v9, v57
	v_pk_fma_f16 v7, v47, v7, v55
	ds_write_b128 v104, v[2:5] offset:47872
	ds_write_b128 v104, v[6:9] offset:65280
	v_pk_add_f16 v39, v2, v6
	v_add_u32_e32 v2, s18, v59
	v_lshl_or_b32 v6, v2, 8, v102
	v_pk_add_f16 v34, v4, v8
	v_pk_add_f16 v37, v3, v7
	v_add_u32_e32 v2, 0x1000, v6
	v_add_u32_e32 v7, 0x2000, v6
	v_add_u32_e32 v8, 0x3000, v6
	v_pk_add_f16 v50, v71, v75
	v_pk_add_f16 v58, v70, v74
	v_pk_add_f16 v119, v69, v73
	v_pk_add_f16 v120, v68, v72
	v_pk_add_f16 v40, v17, v25
	v_pk_add_f16 v42, v16, v24
	v_pk_add_f16 v45, v15, v23
	v_pk_add_f16 v49, v14, v22
	v_pk_add_f16 v32, v5, v9
	buffer_load_dwordx4 v[68:71], v6, s[8:11], 0 offen sc1
	buffer_load_dwordx4 v[72:75], v2, s[8:11], 0 offen sc1
	buffer_load_dwordx4 v[14:17], v7, s[8:11], 0 offen sc1
	s_nop 0
	buffer_load_dwordx4 v[2:5], v8, s[8:11], 0 offen sc1
	v_add_u32_e32 v7, 0x4000, v6
	v_add_u32_e32 v8, 0x5000, v6
	v_add_u32_e32 v59, 0x6000, v6
	buffer_load_dwordx4 v[76:79], v7, s[8:11], 0 offen sc1
	buffer_load_dwordx4 v[80:83], v8, s[8:11], 0 offen sc1
	v_add_u32_e32 v84, 0x7000, v6
	buffer_load_dwordx4 v[22:25], v59, s[8:11], 0 offen sc1
	buffer_load_dwordx4 v[6:9], v84, s[8:11], 0 offen sc1
	v_mov_b32_e32 v59, v0
	v_fma_mix_f32 v192, v114, s44, 0 op_sel_hi:[1,0,0]
	v_fma_mix_f32 v193, v114, s44, 0 op_sel:[1,0,0] op_sel_hi:[1,0,0]
	v_fma_mix_f32 v192, v118, s44, v192 op_sel_hi:[1,0,0]
	v_fma_mix_f32 v193, v118, s44, v193 op_sel:[1,0,0] op_sel_hi:[1,0,0]
	v_fma_mix_f32 v194, v54, s44, 0 op_sel_hi:[1,0,0]
	v_fma_mix_f32 v195, v54, s44, 0 op_sel:[1,0,0] op_sel_hi:[1,0,0]
	v_fma_mix_f32 v194, v117, s44, v194 op_sel_hi:[1,0,0]
	v_fma_mix_f32 v195, v117, s44, v195 op_sel:[1,0,0] op_sel_hi:[1,0,0]
	v_fma_mix_f32 v196, v48, s44, 0 op_sel_hi:[1,0,0]
	v_fma_mix_f32 v197, v48, s44, 0 op_sel:[1,0,0] op_sel_hi:[1,0,0]
	v_fma_mix_f32 v196, v116, s44, v196 op_sel_hi:[1,0,0]
	v_fma_mix_f32 v197, v116, s44, v197 op_sel:[1,0,0] op_sel_hi:[1,0,0]
	v_fma_mix_f32 v198, v44, s44, 0 op_sel_hi:[1,0,0]
	v_fma_mix_f32 v199, v44, s44, 0 op_sel:[1,0,0] op_sel_hi:[1,0,0]
	v_fma_mix_f32 v198, v115, s44, v198 op_sel_hi:[1,0,0]
	v_fma_mix_f32 v199, v115, s44, v199 op_sel:[1,0,0] op_sel_hi:[1,0,0]
	v_fma_mix_f32 v200, v43, s44, 0 op_sel_hi:[1,0,0]
	v_fma_mix_f32 v201, v43, s44, 0 op_sel:[1,0,0] op_sel_hi:[1,0,0]
	v_fma_mix_f32 v200, v120, s44, v200 op_sel_hi:[1,0,0]
	v_fma_mix_f32 v201, v120, s44, v201 op_sel:[1,0,0] op_sel_hi:[1,0,0]
	v_fma_mix_f32 v202, v41, s44, 0 op_sel_hi:[1,0,0]
	v_fma_mix_f32 v203, v41, s44, 0 op_sel:[1,0,0] op_sel_hi:[1,0,0]
	v_fma_mix_f32 v202, v119, s44, v202 op_sel_hi:[1,0,0]
	v_fma_mix_f32 v203, v119, s44, v203 op_sel:[1,0,0] op_sel_hi:[1,0,0]
	v_fma_mix_f32 v204, v38, s44, 0 op_sel_hi:[1,0,0]
	v_fma_mix_f32 v205, v38, s44, 0 op_sel:[1,0,0] op_sel_hi:[1,0,0]
	v_fma_mix_f32 v204, v58, s44, v204 op_sel_hi:[1,0,0]
	v_fma_mix_f32 v205, v58, s44, v205 op_sel:[1,0,0] op_sel_hi:[1,0,0]
	v_fma_mix_f32 v206, v36, s44, 0 op_sel_hi:[1,0,0]
	v_fma_mix_f32 v207, v36, s44, 0 op_sel:[1,0,0] op_sel_hi:[1,0,0]
	v_fma_mix_f32 v206, v50, s44, v206 op_sel_hi:[1,0,0]
	v_fma_mix_f32 v207, v50, s44, v207 op_sel:[1,0,0] op_sel_hi:[1,0,0]
	v_fma_mix_f32 v208, v35, s44, 0 op_sel_hi:[1,0,0]
	v_fma_mix_f32 v209, v35, s44, 0 op_sel:[1,0,0] op_sel_hi:[1,0,0]
	v_fma_mix_f32 v208, v49, s44, v208 op_sel_hi:[1,0,0]
	v_fma_mix_f32 v209, v49, s44, v209 op_sel:[1,0,0] op_sel_hi:[1,0,0]
	v_fma_mix_f32 v210, v33, s44, 0 op_sel_hi:[1,0,0]
	v_fma_mix_f32 v211, v33, s44, 0 op_sel:[1,0,0] op_sel_hi:[1,0,0]
	v_fma_mix_f32 v210, v45, s44, v210 op_sel_hi:[1,0,0]
	v_fma_mix_f32 v211, v45, s44, v211 op_sel:[1,0,0] op_sel_hi:[1,0,0]
	v_fma_mix_f32 v212, v31, s44, 0 op_sel_hi:[1,0,0]
	v_fma_mix_f32 v213, v31, s44, 0 op_sel:[1,0,0] op_sel_hi:[1,0,0]
	v_fma_mix_f32 v212, v42, s44, v212 op_sel_hi:[1,0,0]
	v_fma_mix_f32 v213, v42, s44, v213 op_sel:[1,0,0] op_sel_hi:[1,0,0]
	v_fma_mix_f32 v214, v30, s44, 0 op_sel_hi:[1,0,0]
	v_fma_mix_f32 v215, v30, s44, 0 op_sel:[1,0,0] op_sel_hi:[1,0,0]
	v_fma_mix_f32 v214, v40, s44, v214 op_sel_hi:[1,0,0]
	v_fma_mix_f32 v215, v40, s44, v215 op_sel:[1,0,0] op_sel_hi:[1,0,0]
	v_fma_mix_f32 v216, v29, s44, 0 op_sel_hi:[1,0,0]
	v_fma_mix_f32 v217, v29, s44, 0 op_sel:[1,0,0] op_sel_hi:[1,0,0]
	v_fma_mix_f32 v216, v39, s44, v216 op_sel_hi:[1,0,0]
	v_fma_mix_f32 v217, v39, s44, v217 op_sel:[1,0,0] op_sel_hi:[1,0,0]
	v_fma_mix_f32 v218, v28, s44, 0 op_sel_hi:[1,0,0]
	v_fma_mix_f32 v219, v28, s44, 0 op_sel:[1,0,0] op_sel_hi:[1,0,0]
	v_fma_mix_f32 v218, v37, s44, v218 op_sel_hi:[1,0,0]
	v_fma_mix_f32 v219, v37, s44, v219 op_sel:[1,0,0] op_sel_hi:[1,0,0]
	v_fma_mix_f32 v220, v27, s44, 0 op_sel_hi:[1,0,0]
	v_fma_mix_f32 v221, v27, s44, 0 op_sel:[1,0,0] op_sel_hi:[1,0,0]
	v_fma_mix_f32 v220, v34, s44, v220 op_sel_hi:[1,0,0]
	v_fma_mix_f32 v221, v34, s44, v221 op_sel:[1,0,0] op_sel_hi:[1,0,0]
	v_fma_mix_f32 v222, v26, s44, 0 op_sel_hi:[1,0,0]
	v_fma_mix_f32 v223, v26, s44, 0 op_sel:[1,0,0] op_sel_hi:[1,0,0]
	v_fma_mix_f32 v222, v32, s44, v222 op_sel_hi:[1,0,0]
	v_fma_mix_f32 v223, v32, s44, v223 op_sel:[1,0,0] op_sel_hi:[1,0,0]
	s_waitcnt lgkmcnt(0)
	s_barrier
	s_lshl_b32 s8, s12, 16
	v_add_u32_e32 v85, 0xffffff00, v59
	v_lshlrev_b32_e32 v84, 3, v59
	v_lshrrev_b32_e32 v121, 4, v85
	v_and_b32_e32 v102, 56, v84
	v_lshrrev_b32_e32 v110, 3, v85
	v_ashrrev_i32_e32 v85, 3, v85
	s_movk_i32 s10, 0xffc0
	s_or_b32 s8, s8, s17
	v_lshl_or_b32 v84, v102, 1, v122
	v_bfi_b32 v85, s10, v85, v110
	s_movk_i32 s11, 0x90
	v_or_b32_e32 v106, s8, v102
	v_mad_u64_u32 v[102:103], s[8:9], v85, s11, v[84:85]
	ds_read_b128 v[102:105], v102
	v_lshlrev_b32_e32 v123, 1, v106
	v_lshrrev_b32_e32 v111, 3, v59
	v_ashrrev_i32_e32 v106, 3, v59
	v_lshl_add_u32 v85, v85, 8, v123
	v_bfi_b32 v112, s10, v106, v111
	v_mad_u64_u32 v[106:107], s[8:9], v112, s11, v[84:85]
	ds_read_b128 v[106:109], v106
	s_waitcnt lgkmcnt(1)
	buffer_store_dwordx4 v[102:105], v85, s[4:7], 0 offen sc1
	v_add_u32_e32 v85, 0x100, v59
	v_ashrrev_i32_e32 v85, 3, v85
	v_bfi_b32 v125, s10, v85, v110
	v_mad_u64_u32 v[102:103], s[8:9], v125, s11, v[84:85]
	v_add_u32_e32 v85, 0x200, v59
	v_ashrrev_i32_e32 v85, 3, v85
	v_bfi_b32 v126, s10, v85, v111
	ds_read_b128 v[102:105], v102
	v_mad_u64_u32 v[84:85], s[8:9], v126, s11, v[84:85]
	v_lshl_add_u32 v124, v112, 8, v123
	ds_read_b128 v[110:113], v84
	v_lshl_add_u32 v84, v125, 8, v123
	s_waitcnt lgkmcnt(2)
	buffer_store_dwordx4 v[106:109], v124, s[4:7], 0 offen sc1
	s_waitcnt lgkmcnt(1)
	buffer_store_dwordx4 v[102:105], v84, s[4:7], 0 offen sc1
	v_lshl_add_u32 v84, v126, 8, v123
	v_lshlrev_b32_e32 v59, 4, v59
	s_waitcnt lgkmcnt(0)
	buffer_store_dwordx4 v[110:113], v84, s[4:7], 0 offen sc1
	v_and_b32_e32 v84, 0xf0, v59
	s_waitcnt vmcnt(19)
	v_pk_fma_f16 v63, v52, v63, v57
	v_pk_fma_f16 v62, v51, v62, v56
	v_pk_fma_f16 v61, v47, v61, v55
	v_pk_fma_f16 v60, v46, v60, v53
	s_waitcnt vmcnt(15)
	v_pk_fma_f16 v93, v52, v93, v57
	v_pk_fma_f16 v92, v51, v92, v56
	v_pk_fma_f16 v91, v47, v91, v55
	v_pk_fma_f16 v90, v46, v90, v53
	v_mad_u64_u32 v[84:85], s[8:9], v121, s13, v[84:85]
	ds_write_b128 v84, v[60:63]
	ds_write_b128 v84, v[90:93] offset:17408
	v_pk_add_f16 v59, v63, v93
	v_pk_add_f16 v85, v62, v92
	v_pk_add_f16 v91, v61, v91
	v_pk_add_f16 v90, v60, v90
	v_pk_fma_f16 v63, v52, v67, v57
	v_pk_fma_f16 v62, v51, v66, v56
	v_pk_fma_f16 v61, v47, v65, v55
	v_pk_fma_f16 v60, v46, v64, v53
	s_waitcnt vmcnt(14)
	v_pk_fma_f16 v67, v52, v97, v57
	v_pk_fma_f16 v66, v51, v96, v56
	v_pk_fma_f16 v65, v47, v95, v55
	v_pk_fma_f16 v64, v46, v94, v53
	ds_write_b128 v84, v[60:63] offset:4352
	ds_write_b128 v84, v[64:67] offset:21760
	v_pk_add_f16 v92, v63, v67
	v_pk_add_f16 v93, v62, v66
	v_pk_add_f16 v94, v61, v65
	v_pk_add_f16 v95, v60, v64
	v_pk_fma_f16 v63, v52, v89, v57
	v_pk_fma_f16 v62, v51, v88, v56
	v_pk_fma_f16 v61, v47, v87, v55
	v_pk_fma_f16 v60, v46, v86, v53
	s_waitcnt vmcnt(13)
	v_pk_fma_f16 v67, v52, v101, v57
	v_pk_fma_f16 v66, v51, v100, v56
	v_pk_fma_f16 v65, v47, v99, v55
	v_pk_fma_f16 v64, v46, v98, v53
	ds_write_b128 v84, v[60:63] offset:8704
	ds_write_b128 v84, v[64:67] offset:26112
	v_pk_add_f16 v86, v63, v67
	v_pk_add_f16 v87, v62, v66
	v_pk_add_f16 v88, v61, v65
	v_pk_add_f16 v89, v60, v64
	v_pk_fma_f16 v63, v52, v13, v57
	v_pk_fma_f16 v62, v51, v12, v56
	v_pk_fma_f16 v61, v47, v11, v55
	v_pk_fma_f16 v60, v46, v10, v53
	v_mov_b32_e32 v97, v0
	s_waitcnt vmcnt(12)
	v_pk_fma_f16 v21, v52, v21, v57
	v_pk_fma_f16 v20, v51, v20, v56
	v_pk_fma_f16 v19, v47, v19, v55
	v_pk_fma_f16 v18, v46, v18, v53
	ds_write_b128 v84, v[60:63] offset:13056
	ds_write_b128 v84, v[18:21] offset:30464
	s_waitcnt lgkmcnt(0)
	s_barrier
	v_pk_add_f16 v96, v60, v18
	v_add_u32_e32 v13, 0xffffff00, v97
	v_lshlrev_b32_e32 v12, 3, v97
	v_lshrrev_b32_e32 v98, 4, v13
	v_and_b32_e32 v18, 56, v12
	v_lshrrev_b32_e32 v64, 3, v13
	v_ashrrev_i32_e32 v13, 3, v13
	v_lshl_or_b32 v12, v18, 1, v122
	v_bfi_b32 v13, s10, v13, v64
	v_pk_add_f16 v84, v61, v19
	v_or_b32_e32 v60, s2, v18
	v_mad_u64_u32 v[18:19], s[8:9], v13, s11, v[12:13]
	v_pk_add_f16 v10, v63, v21
	v_pk_add_f16 v11, v62, v20
	ds_read_b128 v[18:21], v18 offset:18432
	v_lshlrev_b32_e32 v99, 1, v60
	v_lshrrev_b32_e32 v65, 3, v97
	v_ashrrev_i32_e32 v60, 3, v97
	v_lshl_add_u32 v13, v13, 8, v99
	v_bfi_b32 v66, s10, v60, v65
	v_mad_u64_u32 v[60:61], s[8:9], v66, s11, v[12:13]
	ds_read_b128 v[60:63], v60 offset:18432
	s_waitcnt lgkmcnt(1)
	buffer_store_dwordx4 v[18:21], v13, s[4:7], 0 offen sc1
	v_add_u32_e32 v13, 0x100, v97
	v_ashrrev_i32_e32 v13, 3, v13
	v_bfi_b32 v101, s10, v13, v64
	v_mad_u64_u32 v[18:19], s[8:9], v101, s11, v[12:13]
	v_add_u32_e32 v13, 0x200, v97
	v_ashrrev_i32_e32 v13, 3, v13
	v_bfi_b32 v102, s10, v13, v65
	ds_read_b128 v[18:21], v18 offset:18432
	v_mad_u64_u32 v[12:13], s[8:9], v102, s11, v[12:13]
	v_lshl_add_u32 v100, v66, 8, v99
	ds_read_b128 v[64:67], v12 offset:18432
	v_lshl_add_u32 v12, v101, 8, v99
	s_waitcnt lgkmcnt(2)
	buffer_store_dwordx4 v[60:63], v100, s[4:7], 0 offen sc1
	s_waitcnt lgkmcnt(1)
	buffer_store_dwordx4 v[18:21], v12, s[4:7], 0 offen sc1
	v_lshl_add_u32 v12, v102, 8, v99
	s_waitcnt lgkmcnt(0)
	buffer_store_dwordx4 v[64:67], v12, s[4:7], 0 offen sc1
	v_lshlrev_b32_e32 v12, 4, v97
	v_and_b32_e32 v12, 0xf0, v12
	s_waitcnt vmcnt(15)
	v_pk_fma_f16 v21, v52, v71, v57
	v_pk_fma_f16 v20, v51, v70, v56
	v_pk_fma_f16 v19, v47, v69, v55
	v_pk_fma_f16 v18, v46, v68, v53
	s_waitcnt vmcnt(11)
	v_pk_fma_f16 v63, v52, v79, v57
	v_pk_fma_f16 v62, v51, v78, v56
	v_pk_fma_f16 v61, v47, v77, v55
	v_pk_fma_f16 v60, v46, v76, v53
	v_mad_u64_u32 v[12:13], s[8:9], v98, s13, v[12:13]
	ds_write_b128 v12, v[18:21] offset:34816
	ds_write_b128 v12, v[60:63] offset:52224
	v_pk_add_f16 v13, v21, v63
	v_pk_add_f16 v64, v20, v62
	v_pk_add_f16 v65, v19, v61
	v_pk_add_f16 v66, v18, v60
	v_pk_fma_f16 v21, v52, v75, v57
	v_pk_fma_f16 v20, v51, v74, v56
	v_pk_fma_f16 v19, v47, v73, v55
	v_pk_fma_f16 v18, v46, v72, v53
	s_waitcnt vmcnt(10)
	v_pk_fma_f16 v63, v52, v83, v57
	v_pk_fma_f16 v62, v51, v82, v56
	v_pk_fma_f16 v61, v47, v81, v55
	v_pk_fma_f16 v60, v46, v80, v53
	v_pk_fma_f16 v17, v52, v17, v57
	v_pk_fma_f16 v16, v51, v16, v56
	v_pk_fma_f16 v15, v47, v15, v55
	v_pk_fma_f16 v14, v46, v14, v53
	v_pk_fma_f16 v5, v52, v5, v57
	v_pk_fma_f16 v4, v51, v4, v56
	v_pk_fma_f16 v3, v47, v3, v55
	v_pk_fma_f16 v2, v46, v2, v53
	s_waitcnt vmcnt(8)
	v_pk_fma_f16 v7, v47, v7, v55
	v_pk_fma_f16 v6, v46, v6, v53
	ds_write_b128 v12, v[18:21] offset:39168
	ds_write_b128 v12, v[60:63] offset:56576
	v_pk_add_f16 v63, v21, v63
	v_pk_add_f16 v62, v20, v62
	v_pk_add_f16 v61, v19, v61
	v_pk_add_f16 v60, v18, v60
	v_pk_fma_f16 v21, v52, v25, v57
	v_pk_fma_f16 v20, v51, v24, v56
	v_pk_fma_f16 v19, v47, v23, v55
	v_pk_fma_f16 v18, v46, v22, v53
	ds_write_b128 v12, v[14:17] offset:43520
	ds_write_b128 v12, v[18:21] offset:60928
	v_pk_fma_f16 v9, v52, v9, v57
	v_pk_fma_f16 v8, v51, v8, v56
	ds_write_b128 v12, v[2:5] offset:47872
	ds_write_b128 v12, v[6:9] offset:65280
	v_pk_add_f16 v24, v3, v7
	v_pk_add_f16 v25, v2, v6
	v_pk_add_f16 v22, v5, v9
	v_pk_add_f16 v23, v4, v8
	v_fma_mix_f32 v192, v90, s44, v192 op_sel_hi:[1,0,0]
	v_fma_mix_f32 v193, v90, s44, v193 op_sel:[1,0,0] op_sel_hi:[1,0,0]
	v_fma_mixlo_f16 v224, v66, s44, v192 op_sel_hi:[1,0,0]
	s_nop 0
	v_fma_mixhi_f16 v224, v66, s44, v193 op_sel:[1,0,0] op_sel_hi:[1,0,0]
	v_pk_add_f16 v19, v15, v19
	v_fma_mix_f32 v194, v91, s44, v194 op_sel_hi:[1,0,0]
	v_fma_mix_f32 v195, v91, s44, v195 op_sel:[1,0,0] op_sel_hi:[1,0,0]
	v_pk_add_f16 v18, v14, v18
	v_fma_mixlo_f16 v225, v65, s44, v194 op_sel_hi:[1,0,0]
	s_nop 0
	v_fma_mixhi_f16 v225, v65, s44, v195 op_sel:[1,0,0] op_sel_hi:[1,0,0]
	s_mov_b32 s2, 0x3e000000
	v_fma_mix_f32 v196, v85, s44, v196 op_sel_hi:[1,0,0]
	v_fma_mix_f32 v197, v85, s44, v197 op_sel:[1,0,0] op_sel_hi:[1,0,0]
	v_fma_mixlo_f16 v226, v64, s44, v196 op_sel_hi:[1,0,0]
	s_nop 0
	v_fma_mixhi_f16 v226, v64, s44, v197 op_sel:[1,0,0] op_sel_hi:[1,0,0]
	v_pk_add_f16 v21, v17, v21
	v_fma_mix_f32 v198, v59, s44, v198 op_sel_hi:[1,0,0]
	v_fma_mix_f32 v199, v59, s44, v199 op_sel:[1,0,0] op_sel_hi:[1,0,0]
	v_pk_add_f16 v20, v16, v20
	v_fma_mixlo_f16 v227, v13, s44, v198 op_sel_hi:[1,0,0]
	s_nop 0
	v_fma_mixhi_f16 v227, v13, s44, v199 op_sel:[1,0,0] op_sel_hi:[1,0,0]
	v_fma_mix_f32 v200, v60, s44, v200 op_sel_hi:[1,0,0]
	v_add_u32_e32 v16, 0x1a000, v12
	v_fma_mix_f32 v201, v60, s44, v201 op_sel:[1,0,0] op_sel_hi:[1,0,0]
	ds_write_b128 v16, v[224:227]
	v_fma_mixlo_f16 v228, v95, s44, v200 op_sel_hi:[1,0,0]
	s_nop 0
	v_fma_mixhi_f16 v228, v95, s44, v201 op_sel:[1,0,0] op_sel_hi:[1,0,0]
	v_fma_mix_f32 v202, v61, s44, v202 op_sel_hi:[1,0,0]
	s_nop 0
	v_fma_mixlo_f16 v229, v94, s44, v202 op_sel_hi:[1,0,0]
	v_fma_mix_f32 v203, v94, s44, v203 op_sel:[1,0,0] op_sel_hi:[1,0,0]
	v_fma_mixhi_f16 v229, v61, s44, v203 op_sel:[1,0,0] op_sel_hi:[1,0,0]
	v_fma_mix_f32 v204, v93, s44, v204 op_sel_hi:[1,0,0]
	v_fma_mix_f32 v205, v93, s44, v205 op_sel:[1,0,0] op_sel_hi:[1,0,0]
	v_fma_mixlo_f16 v230, v62, s44, v204 op_sel_hi:[1,0,0]
	s_nop 0
	v_fma_mixhi_f16 v230, v62, s44, v205 op_sel:[1,0,0] op_sel_hi:[1,0,0]
	v_fma_mix_f32 v206, v63, s44, v206 op_sel_hi:[1,0,0]
	s_nop 0
	v_fma_mixlo_f16 v231, v92, s44, v206 op_sel_hi:[1,0,0]
	v_fma_mix_f32 v207, v92, s44, v207 op_sel:[1,0,0] op_sel_hi:[1,0,0]
	v_fma_mixhi_f16 v231, v63, s44, v207 op_sel:[1,0,0] op_sel_hi:[1,0,0]
	v_fma_mix_f32 v208, v18, s44, v208 op_sel_hi:[1,0,0]
	v_fma_mix_f32 v209, v18, s44, v209 op_sel:[1,0,0] op_sel_hi:[1,0,0]
	v_fma_mix_f32 v210, v19, s44, v210 op_sel_hi:[1,0,0]
	ds_write_b128 v16, v[228:231] offset:4352
	v_fma_mixlo_f16 v232, v89, s44, v208 op_sel_hi:[1,0,0]
	s_nop 0
	v_fma_mixhi_f16 v232, v89, s44, v209 op_sel:[1,0,0] op_sel_hi:[1,0,0]
	v_fma_mix_f32 v211, v19, s44, v211 op_sel:[1,0,0] op_sel_hi:[1,0,0]
	v_fma_mixlo_f16 v233, v88, s44, v210 op_sel_hi:[1,0,0]
	s_nop 0
	v_fma_mixhi_f16 v233, v88, s44, v211 op_sel:[1,0,0] op_sel_hi:[1,0,0]
	v_fma_mix_f32 v212, v87, s44, v212 op_sel_hi:[1,0,0]
	v_fma_mix_f32 v213, v87, s44, v213 op_sel:[1,0,0] op_sel_hi:[1,0,0]
	v_fma_mixlo_f16 v234, v20, s44, v212 op_sel_hi:[1,0,0]
	s_nop 0
	v_fma_mixhi_f16 v234, v20, s44, v213 op_sel:[1,0,0] op_sel_hi:[1,0,0]
	v_fma_mix_f32 v214, v21, s44, v214 op_sel_hi:[1,0,0]
	s_nop 0
	v_fma_mixlo_f16 v235, v86, s44, v214 op_sel_hi:[1,0,0]
	v_fma_mix_f32 v215, v86, s44, v215 op_sel:[1,0,0] op_sel_hi:[1,0,0]
	v_fma_mixhi_f16 v235, v21, s44, v215 op_sel:[1,0,0] op_sel_hi:[1,0,0]
	v_fma_mix_f32 v216, v25, s44, v216 op_sel_hi:[1,0,0]
	v_fma_mix_f32 v217, v25, s44, v217 op_sel:[1,0,0] op_sel_hi:[1,0,0]
	v_fma_mix_f32 v218, v24, s44, v218 op_sel_hi:[1,0,0]
	ds_write_b128 v16, v[232:235] offset:8704
	v_fma_mixlo_f16 v236, v96, s44, v216 op_sel_hi:[1,0,0]
	s_nop 0
	v_fma_mixhi_f16 v236, v96, s44, v217 op_sel:[1,0,0] op_sel_hi:[1,0,0]
	v_fma_mix_f32 v219, v24, s44, v219 op_sel:[1,0,0] op_sel_hi:[1,0,0]
	v_fma_mixlo_f16 v237, v84, s44, v218 op_sel_hi:[1,0,0]
	s_nop 0
	v_fma_mixhi_f16 v237, v84, s44, v219 op_sel:[1,0,0] op_sel_hi:[1,0,0]
	v_fma_mix_f32 v220, v11, s44, v220 op_sel_hi:[1,0,0]
	v_fma_mix_f32 v221, v11, s44, v221 op_sel:[1,0,0] op_sel_hi:[1,0,0]
	v_fma_mixlo_f16 v238, v23, s44, v220 op_sel_hi:[1,0,0]
	s_nop 0
	v_fma_mixhi_f16 v238, v23, s44, v221 op_sel:[1,0,0] op_sel_hi:[1,0,0]
	v_fma_mix_f32 v223, v22, s44, v223 op_sel:[1,0,0] op_sel_hi:[1,0,0]
	v_fma_mix_f32 v222, v10, s44, v222 op_sel_hi:[1,0,0]
	v_fma_mixhi_f16 v239, v10, s44, v223 op_sel:[1,0,0] op_sel_hi:[1,0,0]
	s_nop 0
	v_fma_mixlo_f16 v239, v22, s44, v222 op_sel_hi:[1,0,0]
	s_cmpk_lt_u32 s15, 0x180
	s_cselect_b64 s[8:9], -1, 0
	s_cmpk_gt_u32 s15, 0x17f
	ds_write_b128 v16, v[236:239] offset:13056
	s_cbranch_scc1 .LBB2_3
	s_load_dwordx2 s[10:11], s[0:1], 0x78
	s_load_dwordx4 s[24:27], s[0:1], 0x50
	v_mov_b32_e32 v2, v0
	s_ashr_i32 s13, s12, 31
	s_lshl_b64 s[22:23], s[12:13], 12
	s_waitcnt lgkmcnt(0)
	s_add_u32 s10, s10, s22
	v_lshlrev_b32_e32 v2, 3, v2
	s_addc_u32 s11, s11, s23
	v_and_b32_e32 v2, 0x1f8, v2
	global_load_dwordx2 v[136:137], v2, s[10:11]
	global_load_dwordx2 v[132:133], v2, s[10:11] offset:512
	global_load_dwordx2 v[128:129], v2, s[10:11] offset:1024
	global_load_dwordx2 v[124:125], v2, s[10:11] offset:1536
	global_load_dwordx2 v[134:135], v2, s[10:11] offset:2048
	global_load_dwordx2 v[130:131], v2, s[10:11] offset:2560
	global_load_dwordx2 v[126:127], v2, s[10:11] offset:3072
	global_load_dwordx2 v[122:123], v2, s[10:11] offset:3584
	s_lshl_b32 s2, s14, 4
	s_lshl_b32 s10, s19, 3
	s_add_i32 s10, s10, s2
	s_sub_i32 s2, s10, 32
	s_lshl_b64 s[2:3], s[2:3], 10
	v_lshl_or_b32 v2, v2, 1, s2
	v_mov_b32_e32 v3, s3
	v_lshl_add_u64 v[4:5], s[24:25], 0, v[2:3]
	global_load_dwordx4 v[18:21], v[4:5], off
	global_load_dwordx4 v[102:105], v[4:5], off offset:1024
	global_load_dwordx4 v[94:97], v[4:5], off offset:2048
	global_load_dwordx4 v[86:89], v[4:5], off offset:3072
	v_add_co_u32_e32 v4, vcc, s21, v4
	v_lshl_add_u64 v[6:7], s[26:27], 0, v[2:3]
	s_nop 0
	v_addc_co_u32_e32 v5, vcc, 0, v5, vcc
	global_load_dwordx4 v[78:81], v[4:5], off
	global_load_dwordx4 v[74:77], v[4:5], off offset:1024
	global_load_dwordx4 v[70:73], v[4:5], off offset:2048
	global_load_dwordx4 v[66:69], v[4:5], off offset:3072
	s_nop 0
	global_load_dwordx4 v[2:5], v[6:7], off
	global_load_dwordx4 v[118:121], v[6:7], off offset:1024
	global_load_dwordx4 v[114:117], v[6:7], off offset:2048
	global_load_dwordx4 v[110:113], v[6:7], off offset:3072
	v_add_co_u32_e32 v6, vcc, s21, v6
	s_nop 1
	v_addc_co_u32_e32 v7, vcc, 0, v7, vcc
	global_load_dwordx4 v[106:109], v[6:7], off
	global_load_dwordx4 v[98:101], v[6:7], off offset:1024
	global_load_dwordx4 v[90:93], v[6:7], off offset:2048
	global_load_dwordx4 v[82:85], v[6:7], off offset:3072
	s_branch .LBB2_4

.LBB2_17:
	s_and_b64 vcc, exec, s[2:3]
	s_cbranch_vccz .LBB2_27
	v_mov_b32_e32 v240, 0x64646464
	s_mov_b32 s42, 0x4010400
	s_mov_b32 s43, 0x4030402
	s_load_dwordx2 s[2:3], s[0:1], 0x70
	s_load_dwordx4 s[4:7], s[0:1], 0x40
	s_load_dwordx2 s[36:37], s[0:1], 0x60
	s_lshr_b32 s11, s15, 7
	s_lshl_b32 s8, s12, 3
	s_or_b32 s8, s11, s8
	s_ashr_i32 s9, s8, 31
	s_bfe_u32 s10, s15, 0x10006
	s_lshl_b64 s[12:13], s[8:9], 12
	v_and_b32_e32 v156, 63, v0
	s_waitcnt lgkmcnt(0)
	s_add_u32 s12, s2, s12
	s_addc_u32 s13, s3, s13
	v_lshlrev_b32_e32 v24, 2, v0
	v_and_b32_e32 v24, 0xfc, v24
	v_lshl_or_b32 v24, s14, 8, v24
	global_load_dword v27, v24, s[36:37]
	v_lshlrev_b32_e32 v1, 3, v156
	global_load_dwordx2 v[154:155], v1, s[12:13]
	global_load_dwordx2 v[150:151], v1, s[12:13] offset:512
	global_load_dwordx2 v[146:147], v1, s[12:13] offset:1024
	global_load_dwordx2 v[142:143], v1, s[12:13] offset:1536
	global_load_dwordx2 v[152:153], v1, s[12:13] offset:2048
	global_load_dwordx2 v[148:149], v1, s[12:13] offset:2560
	global_load_dwordx2 v[144:145], v1, s[12:13] offset:3072
	global_load_dwordx2 v[140:141], v1, s[12:13] offset:3584
	s_lshl_b32 s9, s14, 10
	s_lshl_b32 s12, s10, 9
	s_or_b32 s9, s12, s9
	v_or_b32_e32 v1, s9, v156
	v_lshlrev_b32_e32 v2, 4, v1
	v_mov_b32_e32 v3, 0
	v_lshl_add_u64 v[4:5], s[4:5], 0, v[2:3]
	s_movk_i32 s9, 0x1000
	v_add_co_u32_e32 v4, vcc, s9, v4
	v_lshlrev_b32_e32 v1, 2, v0
	s_nop 0
	v_addc_co_u32_e32 v5, vcc, 0, v5, vcc
	global_load_dwordx4 v[86:89], v[4:5], off
	global_load_dwordx4 v[78:81], v[4:5], off offset:1024
	global_load_dwordx4 v[70:73], v[4:5], off offset:2048
	global_load_dwordx4 v[66:69], v[4:5], off offset:3072
	global_load_dwordx4 v[122:125], v2, s[4:5]
	global_load_dwordx4 v[126:129], v2, s[6:7]
	global_load_dwordx4 v[114:117], v2, s[4:5] offset:1024
	global_load_dwordx4 v[118:121], v2, s[6:7] offset:1024
	global_load_dwordx4 v[106:109], v2, s[4:5] offset:2048
	global_load_dwordx4 v[110:113], v2, s[6:7] offset:2048
	global_load_dwordx4 v[98:101], v2, s[4:5] offset:3072
	global_load_dwordx4 v[102:105], v2, s[6:7] offset:3072
	v_lshl_add_u64 v[4:5], s[6:7], 0, v[2:3]
	v_add_co_u32_e32 v2, vcc, 0x1000, v4
	s_nop 1
	v_addc_co_u32_e32 v3, vcc, 0, v5, vcc
	global_load_dwordx4 v[94:97], v[2:3], off
	global_load_dwordx4 v[90:93], v[2:3], off offset:1024
	global_load_dwordx4 v[82:85], v[2:3], off offset:2048
	global_load_dwordx4 v[74:77], v[2:3], off offset:3072
	v_cmp_gt_u32_e32 vcc, 64, v0
	s_and_saveexec_b64 s[4:5], vcc
	s_cbranch_execz .LBB2_20
	v_add_u32_e32 v3, 0x1ee00, v1
	s_waitcnt vmcnt(24)
	ds_write_b32 v3, v27

_Z7k_layerILi0EEvPKDF16_S1_PKfS3_S3_S3_S3_S3_S1_S1_S1_S1_S3_S3_PKhS5_PDF16_S6_PfS7_:
	s_ashr_i32 s3, s2, 1
	s_and_b32 s3, s3, -8
	s_and_b32 s16, s2, 7
	v_readfirstlane_b32 s15, v0
	s_or_b32 s12, s3, s16
	s_bfe_u32 s14, s2, 0x10003
	s_cmpk_gt_u32 s15, 0xff
	s_mov_b64 s[2:3], -1
	s_cbranch_scc0 .LBB3_17
	s_mov_b32 s44, 0x3e000000
	v_mov_b32_e32 v240, 0x64646464
	s_mov_b32 s42, 0x4010400
	s_mov_b32 s43, 0x4030402
	s_load_dwordx4 s[8:11], s[0:1], 0x0
	s_load_dwordx2 s[4:5], s[0:1], 0x80
	v_add_u32_e32 v1, 0xffffff00, v0
	s_ashr_i32 s13, s12, 31
	s_lshr_b32 s17, s15, 6
	v_ashrrev_i32_e32 v2, 4, v1
	v_lshlrev_b32_e32 v3, 3, v0
	s_lshl_b64 s[2:3], s[12:13], 14
	v_and_b32_e32 v82, 0x78, v3
	v_ashrrev_i32_e32 v3, 31, v2
	s_waitcnt lgkmcnt(0)
	s_add_u32 s2, s10, s2
	s_addc_u32 s3, s11, s3
	v_lshlrev_b64 v[4:5], 8, v[2:3]
	v_lshl_add_u64 v[4:5], s[2:3], 0, v[4:5]
	v_lshlrev_b32_e32 v6, 1, v82
	v_mov_b32_e32 v7, 0
	v_lshl_add_u64 v[4:5], v[4:5], 0, v[6:7]
	s_movk_i32 s2, 0x2000
	v_add_co_u32_e32 v8, vcc, s2, v4
	global_load_dwordx4 v[74:77], v[4:5], off
	s_nop 0
	v_addc_co_u32_e32 v9, vcc, 0, v5, vcc
	global_load_dwordx4 v[78:81], v[8:9], off offset:-4096
	global_load_dwordx4 v[66:69], v[8:9], off
	s_movk_i32 s2, 0x3000
	v_add_co_u32_e32 v4, vcc, s2, v4
	s_lshl_b32 s18, s12, 9
	s_nop 0
	v_addc_co_u32_e32 v5, vcc, 0, v5, vcc
	global_load_dwordx4 v[62:65], v[4:5], off
	v_add_u32_e32 v3, s18, v2
	s_mov_b32 s7, 0x20000
	s_mov_b32 s6, 0x1000000
	v_lshl_or_b32 v3, v3, 8, v6
	s_and_b32 s9, s9, 0xffff
	s_mov_b32 s10, s6
	s_mov_b32 s11, s7
	v_add_u32_e32 v4, 0x1000, v3
	buffer_load_dwordx4 v[58:61], v3, s[8:11], 0 offen sc1
	buffer_load_dwordx4 v[50:53], v4, s[8:11], 0 offen sc1
	v_add_u32_e32 v4, 0x2000, v3
	v_add_u32_e32 v5, 0x3000, v3
	buffer_load_dwordx4 v[42:45], v4, s[8:11], 0 offen sc1
	buffer_load_dwordx4 v[34:37], v5, s[8:11], 0 offen sc1
	v_add_u32_e32 v4, 0x4000, v3
	v_add_u32_e32 v5, 0x5000, v3
	buffer_load_dwordx4 v[70:73], v4, s[8:11], 0 offen sc1
	buffer_load_dwordx4 v[54:57], v5, s[8:11], 0 offen sc1
	v_add_u32_e32 v4, 0x6000, v3
	v_add_u32_e32 v3, 0x7000, v3
	buffer_load_dwordx4 v[46:49], v4, s[8:11], 0 offen sc1
	buffer_load_dwordx4 v[38:41], v3, s[8:11], 0 offen sc1
	s_or_b32 s2, s18, 0x80
	v_add_u32_e32 v2, s2, v2
	v_lshl_or_b32 v6, v2, 8, v6
	v_add_u32_e32 v2, 0x1000, v6
	v_add_u32_e32 v7, 0x2000, v6
	v_add_u32_e32 v8, 0x3000, v6
	buffer_load_dwordx4 v[26:29], v6, s[8:11], 0 offen sc1
	buffer_load_dwordx4 v[18:21], v2, s[8:11], 0 offen sc1
	buffer_load_dwordx4 v[10:13], v7, s[8:11], 0 offen sc1
	s_nop 0
	buffer_load_dwordx4 v[2:5], v8, s[8:11], 0 offen sc1
	v_add_u32_e32 v7, 0x4000, v6
	v_add_u32_e32 v8, 0x5000, v6
	v_add_u32_e32 v83, 0x6000, v6
	buffer_load_dwordx4 v[30:33], v7, s[8:11], 0 offen sc1
	buffer_load_dwordx4 v[22:25], v8, s[8:11], 0 offen sc1
	v_add_u32_e32 v84, 0x7000, v6
	buffer_load_dwordx4 v[14:17], v83, s[8:11], 0 offen sc1
	buffer_load_dwordx4 v[6:9], v84, s[8:11], 0 offen sc1
	v_lshlrev_b32_e32 v92, 2, v82
	v_or_b32_e32 v82, 0x1e600, v92
	s_barrier
	ds_read_b128 v[82:85], v82
	v_or_b32_e32 v86, 0x1ea00, v92
	ds_read_b128 v[88:91], v86
	v_or_b32_e32 v93, 0x1e800, v92
	v_or_b32_e32 v102, 0x1ec00, v92
	s_waitcnt lgkmcnt(1)
	v_cvt_pk_f16_f32 v82, v82, v83
	v_cvt_pk_f16_f32 v83, v84, v85
	v_or_b32_e32 v84, 0x1e610, v92
	ds_read_b128 v[84:87], v84
	v_or_b32_e32 v94, 0x1ea10, v92
	v_or_b32_e32 v108, 0x1e810, v92
	v_or_b32_e32 v109, 0x1ec10, v92
	ds_read_b128 v[94:97], v94
	ds_read_b128 v[98:101], v93
	ds_read_b128 v[102:105], v102
	s_waitcnt lgkmcnt(3)
	v_cvt_pk_f16_f32 v84, v84, v85
	s_movk_i32 s22, 0x110
	s_or_b32 s21, s18, 0x100
	s_or_b32 s19, s18, 0x180
	v_mov_b32_e32 v130, v0
	s_lshl_b32 s18, s14, 6
	v_mov_b32_e32 v132, 0x11000
	s_and_b32 s5, s5, 0xffff
	s_lshl_b32 s2, s2, 7
	s_or_b32 s2, s2, s18
	s_mov_b32 s3, 0
	s_movk_i32 s20, 0x1000
	s_waitcnt vmcnt(19)
	v_cvt_f32_f16_e32 v92, v74
	v_cvt_f32_f16_sdwa v93, v74 dst_sel:DWORD dst_unused:UNUSED_PAD src0_sel:WORD_1
	s_waitcnt vmcnt(18)
	v_cvt_f32_f16_e32 v106, v78
	v_cvt_f32_f16_sdwa v107, v78 dst_sel:DWORD dst_unused:UNUSED_PAD src0_sel:WORD_1
	v_cvt_pk_f16_f32 v74, v86, v87
	s_waitcnt lgkmcnt(1)
	v_pk_fma_f32 v[86:87], v[98:99], v[92:93], v[88:89]
	v_pk_fma_f32 v[92:93], v[98:99], v[106:107], v[88:89]
	s_waitcnt lgkmcnt(0)
	v_pk_add_f32 v[92:93], v[102:103], v[92:93]
	s_waitcnt vmcnt(17)
	v_cvt_f32_f16_e32 v106, v66
	v_cvt_f32_f16_sdwa v107, v66 dst_sel:DWORD dst_unused:UNUSED_PAD src0_sel:WORD_1
	v_cvt_pk_f16_f32 v85, v92, v93
	s_waitcnt vmcnt(16)
	v_cvt_f32_f16_e32 v92, v62
	v_cvt_f32_f16_sdwa v93, v62 dst_sel:DWORD dst_unused:UNUSED_PAD src0_sel:WORD_1
	v_cvt_f32_f16_e32 v66, v67
	v_cvt_f32_f16_sdwa v67, v67 dst_sel:DWORD dst_unused:UNUSED_PAD src0_sel:WORD_1
	v_cvt_f32_f16_e32 v62, v63
	v_cvt_f32_f16_sdwa v63, v63 dst_sel:DWORD dst_unused:UNUSED_PAD src0_sel:WORD_1
	v_pk_fma_f32 v[106:107], v[98:99], v[106:107], v[88:89]
	v_pk_fma_f32 v[88:89], v[98:99], v[92:93], v[88:89]
	v_cvt_f32_f16_e32 v92, v75
	v_cvt_f32_f16_sdwa v93, v75 dst_sel:DWORD dst_unused:UNUSED_PAD src0_sel:WORD_1
	v_cvt_f32_f16_e32 v98, v79
	v_cvt_f32_f16_sdwa v99, v79 dst_sel:DWORD dst_unused:UNUSED_PAD src0_sel:WORD_1
	v_pk_add_f32 v[88:89], v[102:103], v[88:89]
	v_pk_fma_f32 v[66:67], v[100:101], v[66:67], v[90:91]
	v_pk_fma_f32 v[62:63], v[100:101], v[62:63], v[90:91]
	v_cvt_pk_f16_f32 v75, v88, v89
	v_pk_fma_f32 v[88:89], v[100:101], v[92:93], v[90:91]
	v_pk_fma_f32 v[92:93], v[100:101], v[98:99], v[90:91]
	v_pk_add_f32 v[66:67], v[104:105], v[66:67]
	v_pk_add_f32 v[62:63], v[104:105], v[62:63]
	v_pk_add_f32 v[86:87], v[102:103], v[86:87]
	v_pk_add_f32 v[106:107], v[102:103], v[106:107]
	v_pk_add_f32 v[88:89], v[104:105], v[88:89]
	v_pk_add_f32 v[92:93], v[104:105], v[92:93]
	v_cvt_pk_f16_f32 v79, v66, v67
	ds_read_b128 v[98:101], v108
	ds_read_b128 v[102:105], v109
	v_cvt_f32_f16_e32 v66, v76
	v_cvt_f32_f16_sdwa v67, v76 dst_sel:DWORD dst_unused:UNUSED_PAD src0_sel:WORD_1
	v_cvt_pk_f16_f32 v76, v62, v63
	v_cvt_f32_f16_e32 v62, v80
	v_cvt_f32_f16_sdwa v63, v80 dst_sel:DWORD dst_unused:UNUSED_PAD src0_sel:WORD_1
	s_waitcnt lgkmcnt(1)
	v_pk_fma_f32 v[66:67], v[98:99], v[66:67], v[94:95]
	v_cvt_pk_f16_f32 v87, v86, v87
	s_waitcnt lgkmcnt(0)
	v_pk_add_f32 v[66:67], v[102:103], v[66:67]
	v_pk_fma_f32 v[62:63], v[98:99], v[62:63], v[94:95]
	v_cvt_pk_f16_f32 v88, v88, v89
	v_pk_add_f32 v[62:63], v[102:103], v[62:63]
	v_cvt_pk_f16_f32 v86, v92, v93
	v_cvt_pk_f16_f32 v92, v66, v67
	v_cvt_f32_f16_e32 v66, v68
	v_cvt_f32_f16_sdwa v67, v68 dst_sel:DWORD dst_unused:UNUSED_PAD src0_sel:WORD_1
	v_cvt_pk_f16_f32 v89, v62, v63
	v_cvt_f32_f16_e32 v62, v64
	v_cvt_f32_f16_sdwa v63, v64 dst_sel:DWORD dst_unused:UNUSED_PAD src0_sel:WORD_1
	v_pk_fma_f32 v[66:67], v[98:99], v[66:67], v[94:95]
	v_cvt_pk_f16_f32 v78, v106, v107
	v_pk_add_f32 v[66:67], v[102:103], v[66:67]
	v_pk_fma_f32 v[62:63], v[98:99], v[62:63], v[94:95]
	v_cvt_pk_f16_f32 v80, v66, v67
	v_pk_add_f32 v[62:63], v[102:103], v[62:63]
	v_cvt_f32_f16_e32 v66, v77
	v_cvt_f32_f16_sdwa v67, v77 dst_sel:DWORD dst_unused:UNUSED_PAD src0_sel:WORD_1
	v_cvt_pk_f16_f32 v77, v62, v63
	v_cvt_f32_f16_e32 v62, v81
	v_cvt_f32_f16_sdwa v63, v81 dst_sel:DWORD dst_unused:UNUSED_PAD src0_sel:WORD_1
	v_pk_fma_f32 v[66:67], v[100:101], v[66:67], v[96:97]
	s_waitcnt vmcnt(15)
	v_pk_fma_f16 v59, v83, v59, v88
	v_pk_add_f32 v[66:67], v[104:105], v[66:67]
	v_pk_fma_f32 v[62:63], v[100:101], v[62:63], v[96:97]
	v_cvt_pk_f16_f32 v95, v66, v67
	v_pk_add_f32 v[62:63], v[104:105], v[62:63]
	v_cvt_f32_f16_e32 v66, v69
	v_cvt_pk_f16_f32 v93, v62, v63
	v_cvt_f32_f16_e32 v62, v65
	v_cvt_f32_f16_sdwa v63, v65 dst_sel:DWORD dst_unused:UNUSED_PAD src0_sel:WORD_1
	v_cvt_f32_f16_sdwa v67, v69 dst_sel:DWORD dst_unused:UNUSED_PAD src0_sel:WORD_1
	v_pk_fma_f16 v61, v74, v61, v95
	v_pk_fma_f16 v58, v82, v58, v87
	v_pk_fma_f32 v[62:63], v[100:101], v[62:63], v[96:97]
	v_pk_fma_f32 v[64:65], v[100:101], v[66:67], v[96:97]
	v_pk_add_f32 v[62:63], v[104:105], v[62:63]
	v_pk_add_f32 v[64:65], v[104:105], v[64:65]
	v_cvt_pk_f16_f32 v81, v62, v63
	v_mov_b32_e32 v62, v0
	v_cvt_pk_f16_f32 v91, v64, v65
	v_add_u32_e32 v63, 0xffffff00, v62
	v_lshlrev_b32_e32 v62, 4, v62
	v_ashrrev_i32_e32 v94, 4, v63
	v_and_b32_e32 v90, 0xf0, v62
	v_pk_fma_f16 v60, v84, v60, v92
	s_waitcnt vmcnt(11)
	v_pk_fma_f16 v62, v82, v70, v87
	v_pk_fma_f16 v51, v83, v51, v86
	v_pk_fma_f16 v53, v74, v53, v93
	v_pk_fma_f16 v50, v82, v50, v85
	v_pk_fma_f16 v52, v84, v52, v89
	v_pk_fma_f16 v43, v83, v43, v79
	v_pk_fma_f16 v45, v74, v45, v91
	v_pk_fma_f16 v42, v82, v42, v78
	v_pk_fma_f16 v44, v84, v44, v80
	v_pk_fma_f16 v35, v83, v35, v76
	v_pk_fma_f16 v37, v74, v37, v81
	v_pk_fma_f16 v34, v82, v34, v75
	v_pk_fma_f16 v36, v84, v36, v77
	s_waitcnt vmcnt(8)
	v_pk_fma_f16 v38, v82, v38, v75
	v_pk_fma_f16 v63, v83, v71, v88
	v_pk_fma_f16 v65, v74, v73, v95
	v_pk_fma_f16 v64, v84, v72, v92
	v_pk_max_f16 v60, v60, 0
	v_pk_max_f16 v58, v58, 0
	v_pk_max_f16 v61, v61, 0
	v_pk_max_f16 v59, v59, 0
	v_pk_max_f16 v62, v62, 0
	v_mad_u64_u32 v[96:97], s[24:25], v94, s22, v[90:91]
	v_pk_fma_f16 v55, v83, v55, v86
	v_pk_fma_f16 v57, v74, v57, v93
	v_pk_fma_f16 v54, v82, v54, v85
	v_pk_fma_f16 v56, v84, v56, v89
	v_pk_max_f16 v52, v52, 0
	v_pk_max_f16 v50, v50, 0
	v_pk_max_f16 v53, v53, 0
	v_pk_max_f16 v51, v51, 0
	v_pk_fma_f16 v47, v83, v47, v79
	v_pk_fma_f16 v49, v74, v49, v91
	v_pk_fma_f16 v46, v82, v46, v78
	v_pk_fma_f16 v48, v84, v48, v80
	v_pk_max_f16 v44, v44, 0
	v_pk_max_f16 v42, v42, 0
	v_pk_max_f16 v45, v45, 0
	v_pk_max_f16 v43, v43, 0
	v_pk_fma_f16 v39, v83, v39, v76
	v_pk_fma_f16 v41, v74, v41, v81
	v_pk_fma_f16 v40, v84, v40, v77
	v_pk_max_f16 v36, v36, 0
	v_pk_max_f16 v34, v34, 0
	v_pk_max_f16 v37, v37, 0
	v_pk_max_f16 v35, v35, 0
	v_pk_max_f16 v38, v38, 0
	v_pk_max_f16 v64, v64, 0
	v_pk_max_f16 v65, v65, 0
	v_pk_max_f16 v63, v63, 0
	ds_write_b128 v96, v[58:61]
	ds_write_b128 v96, v[62:65] offset:17408
	v_pk_add_f16 v73, v58, v62
	v_pk_max_f16 v56, v56, 0
	v_pk_max_f16 v54, v54, 0
	v_pk_max_f16 v57, v57, 0
	v_pk_max_f16 v55, v55, 0
	ds_write_b128 v96, v[50:53] offset:4352
	ds_write_b128 v96, v[54:57] offset:21760
	v_pk_max_f16 v48, v48, 0
	v_pk_max_f16 v46, v46, 0
	v_pk_max_f16 v49, v49, 0
	v_pk_max_f16 v47, v47, 0
	ds_write_b128 v96, v[42:45] offset:8704
	ds_write_b128 v96, v[46:49] offset:26112
	v_pk_max_f16 v40, v40, 0
	v_pk_max_f16 v41, v41, 0
	v_pk_max_f16 v39, v39, 0
	ds_write_b128 v96, v[34:37] offset:13056
	ds_write_b128 v96, v[38:41] offset:30464
	v_pk_add_f16 v62, v34, v38
	v_add_u32_e32 v34, s21, v94
	v_lshl_or_b32 v38, v34, 8, v90
	v_pk_add_f16 v71, v60, v64
	v_pk_add_f16 v60, v35, v39
	v_add_u32_e32 v34, 0x1000, v38
	v_add_u32_e32 v39, 0x2000, v38
	v_pk_add_f16 v69, v61, v65
	v_pk_add_f16 v72, v59, v63
	v_pk_add_f16 v65, v53, v57
	v_pk_add_f16 v67, v52, v56
	v_pk_add_f16 v68, v51, v55
	v_pk_add_f16 v70, v50, v54
	v_pk_add_f16 v61, v45, v49
	v_pk_add_f16 v63, v44, v48
	v_pk_add_f16 v64, v43, v47
	v_pk_add_f16 v66, v42, v46
	v_pk_add_f16 v58, v37, v41
	v_pk_add_f16 v59, v36, v40
	buffer_load_dwordx4 v[100:103], v38, s[8:11], 0 offen sc1
	buffer_load_dwordx4 v[50:53], v34, s[8:11], 0 offen sc1
	v_add_u32_e32 v40, 0x3000, v38
	buffer_load_dwordx4 v[42:45], v39, s[8:11], 0 offen sc1
	buffer_load_dwordx4 v[34:37], v40, s[8:11], 0 offen sc1
	v_add_u32_e32 v39, 0x4000, v38
	v_add_u32_e32 v40, 0x5000, v38
	buffer_load_dwordx4 v[104:107], v39, s[8:11], 0 offen sc1
	buffer_load_dwordx4 v[54:57], v40, s[8:11], 0 offen sc1
	v_add_u32_e32 v90, 0x6000, v38
	v_add_u32_e32 v94, 0x7000, v38
	buffer_load_dwordx4 v[46:49], v90, s[8:11], 0 offen sc1
	buffer_load_dwordx4 v[38:41], v94, s[8:11], 0 offen sc1
	v_mov_b32_e32 v90, v0
	s_waitcnt lgkmcnt(0)
	s_barrier
	s_waitcnt vmcnt(15)
	v_pk_fma_f16 v27, v83, v27, v88
	v_add_u32_e32 v94, 0xffffff00, v90
	v_lshlrev_b32_e32 v90, 4, v90
	v_ashrrev_i32_e32 v109, 4, v94
	v_and_b32_e32 v108, 0xf0, v90
	v_pk_fma_f16 v29, v74, v29, v95
	v_pk_fma_f16 v26, v82, v26, v87
	v_pk_fma_f16 v28, v84, v28, v92
	s_waitcnt vmcnt(11)
	v_pk_fma_f16 v30, v82, v30, v87
	v_pk_fma_f16 v19, v83, v19, v86
	v_pk_fma_f16 v21, v74, v21, v93
	v_pk_fma_f16 v18, v82, v18, v85
	v_pk_fma_f16 v20, v84, v20, v89
	v_pk_fma_f16 v11, v83, v11, v79
	v_pk_fma_f16 v13, v74, v13, v91
	v_pk_fma_f16 v10, v82, v10, v78
	v_pk_fma_f16 v12, v84, v12, v80
	v_pk_fma_f16 v3, v83, v3, v76
	v_pk_fma_f16 v5, v74, v5, v81
	v_pk_fma_f16 v2, v82, v2, v75
	v_pk_fma_f16 v4, v84, v4, v77
	s_waitcnt vmcnt(8)
	v_pk_fma_f16 v6, v82, v6, v75
	v_pk_fma_f16 v31, v83, v31, v88
	v_pk_fma_f16 v33, v74, v33, v95
	v_pk_fma_f16 v32, v84, v32, v92
	v_pk_max_f16 v28, v28, 0
	v_pk_max_f16 v26, v26, 0
	v_pk_max_f16 v29, v29, 0
	v_pk_max_f16 v27, v27, 0
	v_pk_max_f16 v30, v30, 0
	v_mad_u64_u32 v[110:111], s[24:25], v109, s22, v[108:109]
	v_pk_fma_f16 v23, v83, v23, v86
	v_pk_fma_f16 v25, v74, v25, v93
	v_pk_fma_f16 v22, v82, v22, v85
	v_pk_fma_f16 v24, v84, v24, v89
	v_pk_max_f16 v20, v20, 0
	v_pk_max_f16 v18, v18, 0
	v_pk_max_f16 v21, v21, 0
	v_pk_max_f16 v19, v19, 0
	v_pk_fma_f16 v15, v83, v15, v79
	v_pk_fma_f16 v17, v74, v17, v91
	v_pk_fma_f16 v14, v82, v14, v78
	v_pk_fma_f16 v16, v84, v16, v80
	v_pk_max_f16 v12, v12, 0
	v_pk_max_f16 v10, v10, 0
	v_pk_max_f16 v13, v13, 0
	v_pk_max_f16 v11, v11, 0
	v_pk_fma_f16 v7, v83, v7, v76
	v_pk_fma_f16 v9, v74, v9, v81
	v_pk_fma_f16 v8, v84, v8, v77
	v_pk_max_f16 v4, v4, 0
	v_pk_max_f16 v2, v2, 0
	v_pk_max_f16 v5, v5, 0
	v_pk_max_f16 v3, v3, 0
	v_pk_max_f16 v6, v6, 0
	v_pk_max_f16 v32, v32, 0
	v_pk_max_f16 v33, v33, 0
	v_pk_max_f16 v31, v31, 0
	ds_write_b128 v110, v[26:29] offset:34816
	ds_write_b128 v110, v[30:33] offset:52224
	v_pk_add_f16 v129, v26, v30
	v_pk_max_f16 v24, v24, 0
	v_pk_max_f16 v22, v22, 0
	v_pk_max_f16 v25, v25, 0
	v_pk_max_f16 v23, v23, 0
	ds_write_b128 v110, v[18:21] offset:39168
	ds_write_b128 v110, v[22:25] offset:56576
	v_pk_max_f16 v16, v16, 0
	v_pk_max_f16 v14, v14, 0
	v_pk_max_f16 v17, v17, 0
	v_pk_max_f16 v15, v15, 0
	ds_write_b128 v110, v[10:13] offset:43520
	ds_write_b128 v110, v[14:17] offset:60928
	v_pk_max_f16 v8, v8, 0
	v_pk_max_f16 v9, v9, 0
	v_pk_max_f16 v7, v7, 0
	ds_write_b128 v110, v[2:5] offset:47872
	ds_write_b128 v110, v[6:9] offset:65280
	v_pk_add_f16 v30, v2, v6
	v_add_u32_e32 v2, s19, v109
	v_lshl_or_b32 v6, v2, 8, v108
	v_pk_add_f16 v99, v28, v32
	v_pk_add_f16 v128, v27, v31
	v_pk_add_f16 v27, v4, v8
	v_pk_add_f16 v28, v3, v7
	v_add_u32_e32 v2, 0x1000, v6
	v_add_u32_e32 v7, 0x2000, v6
	v_add_u32_e32 v8, 0x3000, v6
	v_pk_add_f16 v97, v29, v33
	v_pk_add_f16 v33, v21, v25
	v_pk_add_f16 v94, v20, v24
	v_pk_add_f16 v96, v19, v23
	v_pk_add_f16 v98, v18, v22
	v_pk_add_f16 v29, v13, v17
	v_pk_add_f16 v31, v12, v16
	v_pk_add_f16 v32, v11, v15
	v_pk_add_f16 v90, v10, v14
	v_pk_add_f16 v26, v5, v9
	buffer_load_dwordx4 v[108:111], v6, s[8:11], 0 offen sc1
	buffer_load_dwordx4 v[18:21], v2, s[8:11], 0 offen sc1
	buffer_load_dwordx4 v[10:13], v7, s[8:11], 0 offen sc1
	s_nop 0
	buffer_load_dwordx4 v[2:5], v8, s[8:11], 0 offen sc1
	v_add_u32_e32 v7, 0x4000, v6
	v_add_u32_e32 v8, 0x5000, v6
	v_add_u32_e32 v116, 0x6000, v6
	buffer_load_dwordx4 v[112:115], v7, s[8:11], 0 offen sc1
	buffer_load_dwordx4 v[22:25], v8, s[8:11], 0 offen sc1
	v_add_u32_e32 v117, 0x7000, v6
	buffer_load_dwordx4 v[14:17], v116, s[8:11], 0 offen sc1
	buffer_load_dwordx4 v[6:9], v117, s[8:11], 0 offen sc1
	v_fma_mix_f32 v192, v73, s44, 0 op_sel_hi:[1,0,0]
	v_fma_mix_f32 v193, v73, s44, 0 op_sel:[1,0,0] op_sel_hi:[1,0,0]
	v_fma_mix_f32 v192, v129, s44, v192 op_sel_hi:[1,0,0]
	v_fma_mix_f32 v193, v129, s44, v193 op_sel:[1,0,0] op_sel_hi:[1,0,0]
	v_fma_mix_f32 v194, v72, s44, 0 op_sel_hi:[1,0,0]
	v_fma_mix_f32 v195, v72, s44, 0 op_sel:[1,0,0] op_sel_hi:[1,0,0]
	v_fma_mix_f32 v194, v128, s44, v194 op_sel_hi:[1,0,0]
	v_fma_mix_f32 v195, v128, s44, v195 op_sel:[1,0,0] op_sel_hi:[1,0,0]
	v_fma_mix_f32 v196, v71, s44, 0 op_sel_hi:[1,0,0]
	v_fma_mix_f32 v197, v71, s44, 0 op_sel:[1,0,0] op_sel_hi:[1,0,0]
	v_fma_mix_f32 v196, v99, s44, v196 op_sel_hi:[1,0,0]
	v_fma_mix_f32 v197, v99, s44, v197 op_sel:[1,0,0] op_sel_hi:[1,0,0]
	v_fma_mix_f32 v198, v69, s44, 0 op_sel_hi:[1,0,0]
	v_fma_mix_f32 v199, v69, s44, 0 op_sel:[1,0,0] op_sel_hi:[1,0,0]
	v_fma_mix_f32 v198, v97, s44, v198 op_sel_hi:[1,0,0]
	v_fma_mix_f32 v199, v97, s44, v199 op_sel:[1,0,0] op_sel_hi:[1,0,0]
	v_fma_mix_f32 v200, v70, s44, 0 op_sel_hi:[1,0,0]
	v_fma_mix_f32 v201, v70, s44, 0 op_sel:[1,0,0] op_sel_hi:[1,0,0]
	v_fma_mix_f32 v200, v98, s44, v200 op_sel_hi:[1,0,0]
	v_fma_mix_f32 v201, v98, s44, v201 op_sel:[1,0,0] op_sel_hi:[1,0,0]
	v_fma_mix_f32 v202, v68, s44, 0 op_sel_hi:[1,0,0]
	v_fma_mix_f32 v203, v68, s44, 0 op_sel:[1,0,0] op_sel_hi:[1,0,0]
	v_fma_mix_f32 v202, v96, s44, v202 op_sel_hi:[1,0,0]
	v_fma_mix_f32 v203, v96, s44, v203 op_sel:[1,0,0] op_sel_hi:[1,0,0]
	v_fma_mix_f32 v204, v67, s44, 0 op_sel_hi:[1,0,0]
	v_fma_mix_f32 v205, v67, s44, 0 op_sel:[1,0,0] op_sel_hi:[1,0,0]
	v_fma_mix_f32 v204, v94, s44, v204 op_sel_hi:[1,0,0]
	v_fma_mix_f32 v205, v94, s44, v205 op_sel:[1,0,0] op_sel_hi:[1,0,0]
	v_fma_mix_f32 v206, v65, s44, 0 op_sel_hi:[1,0,0]
	v_fma_mix_f32 v207, v65, s44, 0 op_sel:[1,0,0] op_sel_hi:[1,0,0]
	v_fma_mix_f32 v206, v33, s44, v206 op_sel_hi:[1,0,0]
	v_fma_mix_f32 v207, v33, s44, v207 op_sel:[1,0,0] op_sel_hi:[1,0,0]
	v_fma_mix_f32 v208, v66, s44, 0 op_sel_hi:[1,0,0]
	v_fma_mix_f32 v209, v66, s44, 0 op_sel:[1,0,0] op_sel_hi:[1,0,0]
	v_fma_mix_f32 v208, v90, s44, v208 op_sel_hi:[1,0,0]
	v_fma_mix_f32 v209, v90, s44, v209 op_sel:[1,0,0] op_sel_hi:[1,0,0]
	v_fma_mix_f32 v210, v64, s44, 0 op_sel_hi:[1,0,0]
	v_fma_mix_f32 v211, v64, s44, 0 op_sel:[1,0,0] op_sel_hi:[1,0,0]
	v_fma_mix_f32 v210, v32, s44, v210 op_sel_hi:[1,0,0]
	v_fma_mix_f32 v211, v32, s44, v211 op_sel:[1,0,0] op_sel_hi:[1,0,0]
	v_fma_mix_f32 v212, v63, s44, 0 op_sel_hi:[1,0,0]
	v_fma_mix_f32 v213, v63, s44, 0 op_sel:[1,0,0] op_sel_hi:[1,0,0]
	v_fma_mix_f32 v212, v31, s44, v212 op_sel_hi:[1,0,0]
	v_fma_mix_f32 v213, v31, s44, v213 op_sel:[1,0,0] op_sel_hi:[1,0,0]
	v_fma_mix_f32 v214, v61, s44, 0 op_sel_hi:[1,0,0]
	v_fma_mix_f32 v215, v61, s44, 0 op_sel:[1,0,0] op_sel_hi:[1,0,0]
	v_fma_mix_f32 v214, v29, s44, v214 op_sel_hi:[1,0,0]
	v_fma_mix_f32 v215, v29, s44, v215 op_sel:[1,0,0] op_sel_hi:[1,0,0]
	v_fma_mix_f32 v216, v62, s44, 0 op_sel_hi:[1,0,0]
	v_fma_mix_f32 v217, v62, s44, 0 op_sel:[1,0,0] op_sel_hi:[1,0,0]
	v_fma_mix_f32 v216, v30, s44, v216 op_sel_hi:[1,0,0]
	v_fma_mix_f32 v217, v30, s44, v217 op_sel:[1,0,0] op_sel_hi:[1,0,0]
	v_fma_mix_f32 v218, v60, s44, 0 op_sel_hi:[1,0,0]
	v_fma_mix_f32 v219, v60, s44, 0 op_sel:[1,0,0] op_sel_hi:[1,0,0]
	v_fma_mix_f32 v218, v28, s44, v218 op_sel_hi:[1,0,0]
	v_fma_mix_f32 v219, v28, s44, v219 op_sel:[1,0,0] op_sel_hi:[1,0,0]
	v_fma_mix_f32 v220, v59, s44, 0 op_sel_hi:[1,0,0]
	v_fma_mix_f32 v221, v59, s44, 0 op_sel:[1,0,0] op_sel_hi:[1,0,0]
	v_fma_mix_f32 v220, v27, s44, v220 op_sel_hi:[1,0,0]
	v_fma_mix_f32 v221, v27, s44, v221 op_sel:[1,0,0] op_sel_hi:[1,0,0]
	v_fma_mix_f32 v222, v58, s44, 0 op_sel_hi:[1,0,0]
	v_fma_mix_f32 v223, v58, s44, 0 op_sel:[1,0,0] op_sel_hi:[1,0,0]
	v_fma_mix_f32 v222, v26, s44, v222 op_sel_hi:[1,0,0]
	v_fma_mix_f32 v223, v26, s44, v223 op_sel:[1,0,0] op_sel_hi:[1,0,0]
	s_waitcnt lgkmcnt(0)
	s_barrier
	s_lshl_b32 s8, s12, 16
	v_add_u32_e32 v116, 0xffffff00, v130
	v_lshlrev_b32_e32 v117, 3, v130
	v_lshrrev_b32_e32 v131, 4, v116
	v_and_b32_e32 v117, 56, v117
	v_lshrrev_b32_e32 v125, 3, v116
	v_ashrrev_i32_e32 v116, 3, v116
	s_movk_i32 s10, 0xffc0
	s_or_b32 s8, s8, s18
	v_lshl_or_b32 v124, v117, 1, v132
	v_bfi_b32 v121, s10, v116, v125
	s_movk_i32 s11, 0x90
	v_or_b32_e32 v120, s8, v117
	v_mad_u64_u32 v[116:117], s[8:9], v121, s11, v[124:125]
	ds_read_b128 v[116:119], v116
	v_lshlrev_b32_e32 v133, 1, v120
	v_lshrrev_b32_e32 v127, 3, v130
	v_ashrrev_i32_e32 v120, 3, v130
	v_bfi_b32 v134, s10, v120, v127
	v_lshl_add_u32 v126, v121, 8, v133
	v_mad_u64_u32 v[120:121], s[8:9], v134, s11, v[124:125]
	ds_read_b128 v[120:123], v120
	s_waitcnt lgkmcnt(1)
	buffer_store_dwordx4 v[116:119], v126, s[4:7], 0 offen sc1
	v_lshl_add_u32 v134, v134, 8, v133
	s_waitcnt vmcnt(16)
	v_pk_fma_f16 v100, v82, v100, v87
	v_add_u32_e32 v116, 0x100, v130
	v_ashrrev_i32_e32 v116, 3, v116
	v_bfi_b32 v135, s10, v116, v125
	v_mad_u64_u32 v[116:117], s[8:9], v135, s11, v[124:125]
	v_add_u32_e32 v125, 0x200, v130
	v_ashrrev_i32_e32 v125, 3, v125
	v_bfi_b32 v136, s10, v125, v127
	ds_read_b128 v[116:119], v116
	v_mad_u64_u32 v[124:125], s[8:9], v136, s11, v[124:125]
	ds_read_b128 v[124:127], v124
	s_waitcnt lgkmcnt(2)
	buffer_store_dwordx4 v[120:123], v134, s[4:7], 0 offen sc1
	v_pk_fma_f16 v101, v83, v101, v88
	v_pk_fma_f16 v102, v84, v102, v92
	v_lshl_add_u32 v120, v135, 8, v133
	s_waitcnt lgkmcnt(1)
	buffer_store_dwordx4 v[116:119], v120, s[4:7], 0 offen sc1
	v_pk_fma_f16 v103, v74, v103, v95
	s_waitcnt vmcnt(17)
	v_pk_fma_f16 v50, v82, v50, v85
	v_lshl_add_u32 v116, v136, 8, v133
	s_waitcnt lgkmcnt(0)
	buffer_store_dwordx4 v[124:127], v116, s[4:7], 0 offen sc1
	v_lshlrev_b32_e32 v116, 4, v130
	v_and_b32_e32 v116, 0xf0, v116
	v_pk_fma_f16 v51, v83, v51, v86
	v_pk_fma_f16 v52, v84, v52, v89
	v_pk_fma_f16 v53, v74, v53, v93
	s_waitcnt vmcnt(14)
	v_pk_fma_f16 v56, v84, v56, v89
	v_pk_fma_f16 v57, v74, v57, v93
	v_pk_fma_f16 v42, v82, v42, v78
	v_pk_fma_f16 v43, v83, v43, v79
	v_pk_fma_f16 v44, v84, v44, v80
	v_pk_fma_f16 v45, v74, v45, v91
	s_waitcnt vmcnt(13)
	v_pk_fma_f16 v46, v82, v46, v78
	v_pk_fma_f16 v47, v83, v47, v79
	v_pk_fma_f16 v104, v82, v104, v87
	v_pk_fma_f16 v105, v83, v105, v88
	v_pk_fma_f16 v106, v84, v106, v92
	v_pk_fma_f16 v107, v74, v107, v95
	v_pk_max_f16 v103, v103, 0
	v_pk_max_f16 v102, v102, 0
	v_pk_max_f16 v101, v101, 0
	v_pk_max_f16 v100, v100, 0
	v_mad_u64_u32 v[116:117], s[8:9], v131, s22, v[116:117]
	v_pk_fma_f16 v54, v82, v54, v85
	v_pk_fma_f16 v55, v83, v55, v86
	v_pk_max_f16 v53, v53, 0
	v_pk_max_f16 v52, v52, 0
	v_pk_max_f16 v51, v51, 0
	v_pk_max_f16 v50, v50, 0
	v_pk_max_f16 v57, v57, 0
	v_pk_max_f16 v56, v56, 0
	v_pk_fma_f16 v48, v84, v48, v80
	v_pk_fma_f16 v49, v74, v49, v91
	v_pk_max_f16 v45, v45, 0
	v_pk_max_f16 v44, v44, 0
	v_pk_max_f16 v43, v43, 0
	v_pk_max_f16 v42, v42, 0
	v_pk_max_f16 v47, v47, 0
	v_pk_max_f16 v46, v46, 0
	v_pk_max_f16 v107, v107, 0
	v_pk_max_f16 v106, v106, 0
	v_pk_max_f16 v105, v105, 0
	v_pk_max_f16 v104, v104, 0
	ds_write_b128 v116, v[100:103]
	ds_write_b128 v116, v[104:107] offset:17408
	v_pk_max_f16 v55, v55, 0
	v_pk_max_f16 v54, v54, 0
	ds_write_b128 v116, v[50:53] offset:4352
	ds_write_b128 v116, v[54:57] offset:21760
	v_pk_add_f16 v53, v53, v57
	v_pk_add_f16 v52, v52, v56
	v_pk_max_f16 v49, v49, 0
	v_pk_max_f16 v48, v48, 0
	ds_write_b128 v116, v[42:45] offset:8704
	ds_write_b128 v116, v[46:49] offset:26112
	v_pk_add_f16 v56, v43, v47
	v_pk_add_f16 v57, v42, v46
	v_pk_fma_f16 v34, v82, v34, v75
	v_pk_fma_f16 v35, v83, v35, v76
	v_pk_fma_f16 v36, v84, v36, v77
	v_pk_fma_f16 v37, v74, v37, v81
	s_waitcnt vmcnt(12)
	v_pk_fma_f16 v42, v82, v38, v75
	v_pk_fma_f16 v43, v83, v39, v76
	v_pk_add_f16 v100, v100, v104
	v_pk_add_f16 v51, v51, v55
	v_pk_add_f16 v50, v50, v54
	v_pk_add_f16 v54, v45, v49
	v_pk_add_f16 v55, v44, v48
	v_pk_fma_f16 v44, v84, v40, v77
	v_pk_fma_f16 v45, v74, v41, v81
	v_pk_max_f16 v41, v37, 0
	v_pk_max_f16 v40, v36, 0
	v_pk_max_f16 v39, v35, 0
	v_pk_max_f16 v38, v34, 0
	v_pk_max_f16 v43, v43, 0
	v_pk_max_f16 v42, v42, 0
	v_mov_b32_e32 v104, v0
	v_pk_max_f16 v45, v45, 0
	v_pk_max_f16 v44, v44, 0
	ds_write_b128 v116, v[38:41] offset:13056
	ds_write_b128 v116, v[42:45] offset:30464
	v_pk_add_f16 v36, v39, v43
	v_pk_add_f16 v37, v38, v42
	s_waitcnt lgkmcnt(0)
	s_barrier
	v_pk_add_f16 v101, v101, v105
	v_add_u32_e32 v38, 0xffffff00, v104
	v_lshlrev_b32_e32 v39, 3, v104
	v_lshrrev_b32_e32 v105, 4, v38
	v_and_b32_e32 v39, 56, v39
	v_lshrrev_b32_e32 v47, 3, v38
	v_ashrrev_i32_e32 v38, 3, v38
	v_lshl_or_b32 v46, v39, 1, v132
	v_bfi_b32 v43, s10, v38, v47
	v_or_b32_e32 v42, s2, v39
	v_mad_u64_u32 v[38:39], s[8:9], v43, s11, v[46:47]
	v_pk_add_f16 v34, v41, v45
	v_pk_add_f16 v35, v40, v44
	ds_read_b128 v[38:41], v38 offset:18432
	v_pk_add_f16 v102, v102, v106
	v_lshlrev_b32_e32 v106, 1, v42
	v_lshrrev_b32_e32 v49, 3, v104
	v_ashrrev_i32_e32 v42, 3, v104
	v_pk_add_f16 v103, v103, v107
	v_bfi_b32 v107, s10, v42, v49
	v_lshl_add_u32 v48, v43, 8, v106
	v_mad_u64_u32 v[42:43], s[8:9], v107, s11, v[46:47]
	ds_read_b128 v[42:45], v42 offset:18432
	s_waitcnt lgkmcnt(1)
	buffer_store_dwordx4 v[38:41], v48, s[4:7], 0 offen sc1
	v_lshl_add_u32 v107, v107, 8, v106
	s_waitcnt vmcnt(11)
	v_pk_fma_f16 v18, v82, v18, v85
	v_add_u32_e32 v38, 0x100, v104
	v_ashrrev_i32_e32 v38, 3, v38
	v_bfi_b32 v116, s10, v38, v47
	v_mad_u64_u32 v[38:39], s[8:9], v116, s11, v[46:47]
	v_add_u32_e32 v47, 0x200, v104
	v_ashrrev_i32_e32 v47, 3, v47
	v_bfi_b32 v117, s10, v47, v49
	ds_read_b128 v[38:41], v38 offset:18432
	v_mad_u64_u32 v[46:47], s[8:9], v117, s11, v[46:47]
	ds_read_b128 v[46:49], v46 offset:18432
	s_waitcnt lgkmcnt(2)
	buffer_store_dwordx4 v[42:45], v107, s[4:7], 0 offen sc1
	v_pk_fma_f16 v19, v83, v19, v86
	v_pk_fma_f16 v20, v84, v20, v89
	v_lshl_add_u32 v42, v116, 8, v106
	s_waitcnt lgkmcnt(1)
	buffer_store_dwordx4 v[38:41], v42, s[4:7], 0 offen sc1
	v_pk_fma_f16 v21, v74, v21, v93
	s_waitcnt vmcnt(9)
	v_pk_fma_f16 v24, v84, v24, v89
	v_lshl_add_u32 v38, v117, 8, v106
	s_waitcnt lgkmcnt(0)
	buffer_store_dwordx4 v[46:49], v38, s[4:7], 0 offen sc1
	v_lshlrev_b32_e32 v38, 4, v104
	v_pk_fma_f16 v39, v83, v109, v88
	v_and_b32_e32 v46, 0xf0, v38
	v_pk_fma_f16 v38, v82, v108, v87
	v_pk_fma_f16 v40, v84, v110, v92
	v_pk_fma_f16 v41, v74, v111, v95
	v_pk_fma_f16 v25, v74, v25, v93
	v_pk_fma_f16 v10, v82, v10, v78
	v_pk_fma_f16 v11, v83, v11, v79
	v_pk_fma_f16 v12, v84, v12, v80
	v_pk_fma_f16 v13, v74, v13, v91
	v_pk_fma_f16 v2, v82, v2, v75
	v_pk_fma_f16 v3, v83, v3, v76
	v_pk_fma_f16 v4, v84, v4, v77
	v_pk_fma_f16 v5, v74, v5, v81
	s_waitcnt vmcnt(8)
	v_pk_fma_f16 v6, v82, v6, v75
	v_pk_fma_f16 v7, v83, v7, v76
	v_pk_fma_f16 v42, v82, v112, v87
	v_pk_fma_f16 v43, v83, v113, v88
	v_pk_fma_f16 v44, v84, v114, v92
	v_pk_fma_f16 v45, v74, v115, v95
	v_pk_max_f16 v41, v41, 0
	v_pk_max_f16 v40, v40, 0
	v_pk_max_f16 v39, v39, 0
	v_pk_max_f16 v38, v38, 0
	v_mad_u64_u32 v[46:47], s[8:9], v105, s22, v[46:47]
	v_pk_fma_f16 v22, v82, v22, v85
	v_pk_fma_f16 v23, v83, v23, v86
	v_pk_max_f16 v21, v21, 0
	v_pk_max_f16 v20, v20, 0
	v_pk_max_f16 v19, v19, 0
	v_pk_max_f16 v18, v18, 0
	v_pk_max_f16 v25, v25, 0
	v_pk_max_f16 v24, v24, 0
	v_pk_fma_f16 v14, v82, v14, v78
	v_pk_fma_f16 v15, v83, v15, v79
	v_pk_fma_f16 v16, v84, v16, v80
	v_pk_fma_f16 v17, v74, v17, v91
	v_pk_max_f16 v13, v13, 0
	v_pk_max_f16 v12, v12, 0
	v_pk_max_f16 v11, v11, 0
	v_pk_max_f16 v10, v10, 0
	v_pk_fma_f16 v8, v84, v8, v77
	v_pk_fma_f16 v9, v74, v9, v81
	v_pk_max_f16 v5, v5, 0
	v_pk_max_f16 v4, v4, 0
	v_pk_max_f16 v3, v3, 0
	v_pk_max_f16 v2, v2, 0
	v_pk_max_f16 v7, v7, 0
	v_pk_max_f16 v6, v6, 0
	v_pk_max_f16 v45, v45, 0
	v_pk_max_f16 v44, v44, 0
	v_pk_max_f16 v43, v43, 0
	v_pk_max_f16 v42, v42, 0
	ds_write_b128 v46, v[38:41] offset:34816
	ds_write_b128 v46, v[42:45] offset:52224
	v_pk_max_f16 v23, v23, 0
	v_pk_max_f16 v22, v22, 0
	ds_write_b128 v46, v[18:21] offset:39168
	ds_write_b128 v46, v[22:25] offset:56576
	v_pk_add_f16 v21, v21, v25
	v_pk_add_f16 v20, v20, v24
	v_pk_max_f16 v17, v17, 0
	v_pk_max_f16 v16, v16, 0
	v_pk_max_f16 v15, v15, 0
	v_pk_max_f16 v14, v14, 0
	ds_write_b128 v46, v[10:13] offset:43520
	ds_write_b128 v46, v[14:17] offset:60928
	v_pk_max_f16 v9, v9, 0
	v_pk_max_f16 v8, v8, 0
	ds_write_b128 v46, v[2:5] offset:47872
	ds_write_b128 v46, v[6:9] offset:65280
	v_pk_add_f16 v24, v3, v7
	v_pk_add_f16 v25, v2, v6
	v_pk_add_f16 v19, v19, v23
	v_pk_add_f16 v18, v18, v22
	v_pk_add_f16 v22, v5, v9
	v_pk_add_f16 v23, v4, v8
	v_pk_add_f16 v38, v38, v42
	v_fma_mix_f32 v192, v100, s44, v192 op_sel_hi:[1,0,0]
	v_fma_mix_f32 v193, v100, s44, v193 op_sel:[1,0,0] op_sel_hi:[1,0,0]
	v_fma_mixlo_f16 v224, v38, s44, v192 op_sel_hi:[1,0,0]
	s_nop 0
	v_fma_mixhi_f16 v224, v38, s44, v193 op_sel:[1,0,0] op_sel_hi:[1,0,0]
	v_pk_add_f16 v39, v39, v43
	v_fma_mix_f32 v194, v101, s44, v194 op_sel_hi:[1,0,0]
	v_fma_mix_f32 v195, v101, s44, v195 op_sel:[1,0,0] op_sel_hi:[1,0,0]
	v_pk_add_f16 v15, v11, v15
	v_pk_add_f16 v14, v10, v14
	v_fma_mixlo_f16 v225, v39, s44, v194 op_sel_hi:[1,0,0]
	s_nop 0
	v_fma_mixhi_f16 v225, v39, s44, v195 op_sel:[1,0,0] op_sel_hi:[1,0,0]
	s_mov_b32 s2, 0x3e000000
	v_pk_add_f16 v40, v40, v44
	v_fma_mix_f32 v196, v102, s44, v196 op_sel_hi:[1,0,0]
	v_fma_mix_f32 v197, v102, s44, v197 op_sel:[1,0,0] op_sel_hi:[1,0,0]
	v_fma_mixlo_f16 v226, v40, s44, v196 op_sel_hi:[1,0,0]
	s_nop 0
	v_fma_mixhi_f16 v226, v40, s44, v197 op_sel:[1,0,0] op_sel_hi:[1,0,0]
	v_pk_add_f16 v41, v41, v45
	v_fma_mix_f32 v198, v103, s44, v198 op_sel_hi:[1,0,0]
	v_fma_mix_f32 v199, v103, s44, v199 op_sel:[1,0,0] op_sel_hi:[1,0,0]
	v_pk_add_f16 v17, v13, v17
	v_pk_add_f16 v16, v12, v16
	v_fma_mixlo_f16 v227, v41, s44, v198 op_sel_hi:[1,0,0]
	s_nop 0
	v_fma_mixhi_f16 v227, v41, s44, v199 op_sel:[1,0,0] op_sel_hi:[1,0,0]
	v_add_u32_e32 v38, 0x1a000, v46
	v_fma_mix_f32 v200, v18, s44, v200 op_sel_hi:[1,0,0]
	v_fma_mix_f32 v201, v18, s44, v201 op_sel:[1,0,0] op_sel_hi:[1,0,0]
	ds_write_b128 v38, v[224:227]
	v_fma_mixlo_f16 v228, v50, s44, v200 op_sel_hi:[1,0,0]
	s_nop 0
	v_fma_mixhi_f16 v228, v50, s44, v201 op_sel:[1,0,0] op_sel_hi:[1,0,0]
	v_fma_mix_f32 v202, v19, s44, v202 op_sel_hi:[1,0,0]
	s_nop 0
	v_fma_mixlo_f16 v229, v51, s44, v202 op_sel_hi:[1,0,0]
	v_fma_mix_f32 v203, v51, s44, v203 op_sel:[1,0,0] op_sel_hi:[1,0,0]
	v_fma_mixhi_f16 v229, v19, s44, v203 op_sel:[1,0,0] op_sel_hi:[1,0,0]
	v_fma_mix_f32 v204, v52, s44, v204 op_sel_hi:[1,0,0]
	v_fma_mix_f32 v205, v52, s44, v205 op_sel:[1,0,0] op_sel_hi:[1,0,0]
	v_fma_mixlo_f16 v230, v20, s44, v204 op_sel_hi:[1,0,0]
	s_nop 0
	v_fma_mixhi_f16 v230, v20, s44, v205 op_sel:[1,0,0] op_sel_hi:[1,0,0]
	v_fma_mix_f32 v206, v21, s44, v206 op_sel_hi:[1,0,0]
	s_nop 0
	v_fma_mixlo_f16 v231, v53, s44, v206 op_sel_hi:[1,0,0]
	v_fma_mix_f32 v207, v53, s44, v207 op_sel:[1,0,0] op_sel_hi:[1,0,0]
	v_fma_mixhi_f16 v231, v21, s44, v207 op_sel:[1,0,0] op_sel_hi:[1,0,0]
	v_fma_mix_f32 v208, v14, s44, v208 op_sel_hi:[1,0,0]
	v_fma_mix_f32 v209, v14, s44, v209 op_sel:[1,0,0] op_sel_hi:[1,0,0]
	v_fma_mix_f32 v210, v15, s44, v210 op_sel_hi:[1,0,0]
	ds_write_b128 v38, v[228:231] offset:4352
	v_fma_mixlo_f16 v232, v57, s44, v208 op_sel_hi:[1,0,0]
	s_nop 0
	v_fma_mixhi_f16 v232, v57, s44, v209 op_sel:[1,0,0] op_sel_hi:[1,0,0]
	v_fma_mix_f32 v211, v15, s44, v211 op_sel:[1,0,0] op_sel_hi:[1,0,0]
	v_fma_mixlo_f16 v233, v56, s44, v210 op_sel_hi:[1,0,0]
	s_nop 0
	v_fma_mixhi_f16 v233, v56, s44, v211 op_sel:[1,0,0] op_sel_hi:[1,0,0]
	v_fma_mix_f32 v212, v55, s44, v212 op_sel_hi:[1,0,0]
	v_fma_mix_f32 v213, v55, s44, v213 op_sel:[1,0,0] op_sel_hi:[1,0,0]
	v_fma_mixlo_f16 v234, v16, s44, v212 op_sel_hi:[1,0,0]
	s_nop 0
	v_fma_mixhi_f16 v234, v16, s44, v213 op_sel:[1,0,0] op_sel_hi:[1,0,0]
	v_fma_mix_f32 v214, v17, s44, v214 op_sel_hi:[1,0,0]
	s_nop 0
	v_fma_mixlo_f16 v235, v54, s44, v214 op_sel_hi:[1,0,0]
	v_fma_mix_f32 v215, v54, s44, v215 op_sel:[1,0,0] op_sel_hi:[1,0,0]
	v_fma_mixhi_f16 v235, v17, s44, v215 op_sel:[1,0,0] op_sel_hi:[1,0,0]
	v_fma_mix_f32 v216, v25, s44, v216 op_sel_hi:[1,0,0]
	v_fma_mix_f32 v217, v25, s44, v217 op_sel:[1,0,0] op_sel_hi:[1,0,0]
	v_fma_mix_f32 v218, v24, s44, v218 op_sel_hi:[1,0,0]
	ds_write_b128 v38, v[232:235] offset:8704
	v_fma_mixlo_f16 v236, v37, s44, v216 op_sel_hi:[1,0,0]
	s_nop 0
	v_fma_mixhi_f16 v236, v37, s44, v217 op_sel:[1,0,0] op_sel_hi:[1,0,0]
	v_fma_mix_f32 v219, v24, s44, v219 op_sel:[1,0,0] op_sel_hi:[1,0,0]
	v_fma_mixlo_f16 v237, v36, s44, v218 op_sel_hi:[1,0,0]
	s_nop 0
	v_fma_mixhi_f16 v237, v36, s44, v219 op_sel:[1,0,0] op_sel_hi:[1,0,0]
	v_fma_mix_f32 v220, v35, s44, v220 op_sel_hi:[1,0,0]
	v_fma_mix_f32 v221, v35, s44, v221 op_sel:[1,0,0] op_sel_hi:[1,0,0]
	v_fma_mixlo_f16 v238, v23, s44, v220 op_sel_hi:[1,0,0]
	s_nop 0
	v_fma_mixhi_f16 v238, v23, s44, v221 op_sel:[1,0,0] op_sel_hi:[1,0,0]
	v_fma_mix_f32 v222, v22, s44, v222 op_sel_hi:[1,0,0]
	s_nop 0
	v_fma_mixlo_f16 v239, v34, s44, v222 op_sel_hi:[1,0,0]
	v_fma_mix_f32 v223, v34, s44, v223 op_sel:[1,0,0] op_sel_hi:[1,0,0]
	v_fma_mixhi_f16 v239, v22, s44, v223 op_sel:[1,0,0] op_sel_hi:[1,0,0]
	s_cmpk_lt_u32 s15, 0x180
	s_cselect_b64 s[8:9], -1, 0
	s_cmpk_gt_u32 s15, 0x17f
	ds_write_b128 v38, v[236:239] offset:13056
	s_cbranch_scc1 .LBB3_3
	s_load_dwordx2 s[10:11], s[0:1], 0x78
	s_load_dwordx4 s[24:27], s[0:1], 0x50
	v_mov_b32_e32 v2, v0
	s_lshl_b64 s[22:23], s[12:13], 12
	s_waitcnt lgkmcnt(0)
	s_add_u32 s10, s10, s22
	v_lshlrev_b32_e32 v2, 3, v2
	s_addc_u32 s11, s11, s23
	v_and_b32_e32 v2, 0x1f8, v2
	global_load_dwordx2 v[136:137], v2, s[10:11]
	global_load_dwordx2 v[132:133], v2, s[10:11] offset:512
	global_load_dwordx2 v[128:129], v2, s[10:11] offset:1024
	global_load_dwordx2 v[124:125], v2, s[10:11] offset:1536
	global_load_dwordx2 v[134:135], v2, s[10:11] offset:2048
	global_load_dwordx2 v[130:131], v2, s[10:11] offset:2560
	global_load_dwordx2 v[126:127], v2, s[10:11] offset:3072
	global_load_dwordx2 v[122:123], v2, s[10:11] offset:3584
	s_lshl_b32 s2, s14, 4
	s_lshl_b32 s10, s17, 3
	s_add_i32 s10, s10, s2
	s_sub_i32 s2, s10, 32
	s_lshl_b64 s[2:3], s[2:3], 10
	v_lshl_or_b32 v2, v2, 1, s2
	v_mov_b32_e32 v3, s3
	v_lshl_add_u64 v[4:5], s[24:25], 0, v[2:3]
	global_load_dwordx4 v[18:21], v[4:5], off
	global_load_dwordx4 v[102:105], v[4:5], off offset:1024
	global_load_dwordx4 v[94:97], v[4:5], off offset:2048
	global_load_dwordx4 v[86:89], v[4:5], off offset:3072
	v_add_co_u32_e32 v4, vcc, s20, v4
	v_lshl_add_u64 v[6:7], s[26:27], 0, v[2:3]
	s_nop 0
	v_addc_co_u32_e32 v5, vcc, 0, v5, vcc
	global_load_dwordx4 v[78:81], v[4:5], off
	global_load_dwordx4 v[74:77], v[4:5], off offset:1024
	global_load_dwordx4 v[70:73], v[4:5], off offset:2048
	global_load_dwordx4 v[66:69], v[4:5], off offset:3072
	s_nop 0
	global_load_dwordx4 v[2:5], v[6:7], off
	global_load_dwordx4 v[118:121], v[6:7], off offset:1024
	global_load_dwordx4 v[114:117], v[6:7], off offset:2048
	global_load_dwordx4 v[110:113], v[6:7], off offset:3072
	v_add_co_u32_e32 v6, vcc, s20, v6
	s_nop 1
	v_addc_co_u32_e32 v7, vcc, 0, v7, vcc
	global_load_dwordx4 v[106:109], v[6:7], off
	global_load_dwordx4 v[98:101], v[6:7], off offset:1024
	global_load_dwordx4 v[90:93], v[6:7], off offset:2048
	global_load_dwordx4 v[82:85], v[6:7], off offset:3072
	s_branch .LBB3_4
